# GEMM K-loops (P2,P8,P12,P17,P19): LDS-DMA loads use scalar base + 32-bit lane offset; 16 v_lshl_add_u64 per iteration removed from the loader segments
# speedup vs baseline: 1.0061x; 1.0061x over previous
.LBB0_202:
	ds_read_b128 v[2:5], v172
	ds_read_b128 v[6:9], v172 offset:1024
	ds_read_b128 v[10:13], v172 offset:2048
	ds_read_b128 v[14:17], v172 offset:3072
	s_add_u32 s34, s30, 0xfffc0080
	s_addc_u32 s35, s31, -1
	s_cmp_eq_u32 s56, 12
	s_cselect_b32 s37, s21, s35
	s_cselect_b32 s36, s52, s34
	s_cselect_b32 s35, s11, s55
	s_cselect_b32 s34, s53, s54
	s_add_i32 m0, s29, 0xc000
	ds_read_b128 v[176:179], v173
	ds_read_b128 v[180:183], v173 offset:1024
	ds_read_b128 v[184:187], v173 offset:2048
	ds_read_b128 v[188:191], v173 offset:3072
	ds_read_b128 v[192:195], v173 offset:4096
	ds_read_b128 v[196:199], v173 offset:5120
	ds_read_b128 v[206:209], v173 offset:6144
	ds_read_b128 v[210:213], v173 offset:7168
	global_load_lds_dwordx4 v154, s[30:31]
	s_add_i32 m0, s29, 0xe000
	s_nop 0
	global_load_lds_dwordx4 v156, s[30:31]
	s_waitcnt lgkmcnt(8)
	s_barrier
	s_waitcnt lgkmcnt(0)
	s_setprio 1
	s_waitcnt lgkmcnt(0)
	v_mfma_scale_f32_16x16x128_f8f6f4 v[142:145], v[2:9], v[176:183], v[142:145], v174, v174 op_sel_hi:[0,0,0]
	v_mfma_scale_f32_16x16x128_f8f6f4 v[138:141], v[10:17], v[176:183], v[138:141], v174, v174 op_sel_hi:[0,0,0]
	v_mfma_scale_f32_16x16x128_f8f6f4 v[134:137], v[2:9], v[184:191], v[134:137], v174, v174 op_sel_hi:[0,0,0]
	v_mfma_scale_f32_16x16x128_f8f6f4 v[126:129], v[10:17], v[184:191], v[126:129], v174, v174 op_sel_hi:[0,0,0]
	v_mfma_scale_f32_16x16x128_f8f6f4 v[118:121], v[2:9], v[192:199], v[118:121], v174, v174 op_sel_hi:[0,0,0]
	v_mfma_scale_f32_16x16x128_f8f6f4 v[110:113], v[10:17], v[192:199], v[110:113], v174, v174 op_sel_hi:[0,0,0]
	v_mfma_scale_f32_16x16x128_f8f6f4 v[102:105], v[2:9], v[206:213], v[102:105], v174, v174 op_sel_hi:[0,0,0]
	v_mfma_scale_f32_16x16x128_f8f6f4 v[94:97], v[10:17], v[206:213], v[94:97], v174, v174 op_sel_hi:[0,0,0]
	s_setprio 0
	s_barrier
	s_add_i32 s57, s48, s38
	s_add_u32 s66, s34, 0x80
	s_addc_u32 s67, s35, 0
	s_mov_b32 m0, s57
	ds_read_b128 v[214:217], v175
	ds_read_b128 v[218:221], v175 offset:1024
	ds_read_b128 v[222:225], v175 offset:2048
	ds_read_b128 v[226:229], v175 offset:3072
	global_load_lds_dwordx4 v150, s[34:35]
	s_add_i32 m0, s57, 0x2000
	s_nop 0
	global_load_lds_dwordx4 v146, s[34:35]
	s_barrier
	s_waitcnt lgkmcnt(0)
	s_setprio 1
	s_waitcnt lgkmcnt(0)
	v_mfma_scale_f32_16x16x128_f8f6f4 v[130:133], v[214:221], v[176:183], v[130:133], v174, v174 op_sel_hi:[0,0,0]
	v_mfma_scale_f32_16x16x128_f8f6f4 v[122:125], v[222:229], v[176:183], v[122:125], v174, v174 op_sel_hi:[0,0,0]
	v_mfma_scale_f32_16x16x128_f8f6f4 v[114:117], v[214:221], v[184:191], v[114:117], v174, v174 op_sel_hi:[0,0,0]
	v_mfma_scale_f32_16x16x128_f8f6f4 v[106:109], v[222:229], v[184:191], v[106:109], v174, v174 op_sel_hi:[0,0,0]
	v_mfma_scale_f32_16x16x128_f8f6f4 v[98:101], v[214:221], v[192:199], v[98:101], v174, v174 op_sel_hi:[0,0,0]
	v_mfma_scale_f32_16x16x128_f8f6f4 v[90:93], v[222:229], v[192:199], v[90:93], v174, v174 op_sel_hi:[0,0,0]
	v_mfma_scale_f32_16x16x128_f8f6f4 v[86:89], v[214:221], v[206:213], v[86:89], v174, v174 op_sel_hi:[0,0,0]
	v_mfma_scale_f32_16x16x128_f8f6f4 v[82:85], v[222:229], v[206:213], v[82:85], v174, v174 op_sel_hi:[0,0,0]
	s_setprio 0
	s_mov_b32 m0, s29
	s_add_u32 s68, s36, 0x80
	s_addc_u32 s69, s37, 0
	s_barrier
	ds_read_b128 v[176:179], v173 offset:16384
	ds_read_b128 v[180:183], v173 offset:17408
	ds_read_b128 v[184:187], v173 offset:18432
	ds_read_b128 v[188:191], v173 offset:19456
	ds_read_b128 v[192:195], v173 offset:20480
	ds_read_b128 v[196:199], v173 offset:21504
	ds_read_b128 v[206:209], v173 offset:22528
	ds_read_b128 v[210:213], v173 offset:23552
	global_load_lds_dwordx4 v152, s[36:37]
	s_mov_b32 m0, s41
	s_nop 0
	global_load_lds_dwordx4 v148, s[36:37]
	s_barrier
	s_waitcnt lgkmcnt(0)
	s_setprio 1
	s_waitcnt lgkmcnt(0)
	v_mfma_scale_f32_16x16x128_f8f6f4 v[78:81], v[2:9], v[176:183], v[78:81], v174, v174 op_sel_hi:[0,0,0]
	v_mfma_scale_f32_16x16x128_f8f6f4 v[74:77], v[10:17], v[176:183], v[74:77], v174, v174 op_sel_hi:[0,0,0]
	v_mfma_scale_f32_16x16x128_f8f6f4 v[70:73], v[2:9], v[184:191], v[70:73], v174, v174 op_sel_hi:[0,0,0]
	v_mfma_scale_f32_16x16x128_f8f6f4 v[62:65], v[10:17], v[184:191], v[62:65], v174, v174 op_sel_hi:[0,0,0]
	v_mfma_scale_f32_16x16x128_f8f6f4 v[54:57], v[2:9], v[192:199], v[54:57], v174, v174 op_sel_hi:[0,0,0]
	v_mfma_scale_f32_16x16x128_f8f6f4 v[46:49], v[10:17], v[192:199], v[46:49], v174, v174 op_sel_hi:[0,0,0]
	v_mfma_scale_f32_16x16x128_f8f6f4 v[38:41], v[2:9], v[206:213], v[38:41], v174, v174 op_sel_hi:[0,0,0]
	v_mfma_scale_f32_16x16x128_f8f6f4 v[30:33], v[10:17], v[206:213], v[30:33], v174, v174 op_sel_hi:[0,0,0]
	s_setprio 0
	s_barrier
	s_add_u32 s60, s34, 0x40000
	s_addc_u32 s61, s35, 0
	s_add_i32 s57, s49, s38
	s_mov_b32 m0, s57
	s_nop 0
	global_load_lds_dwordx4 v150, s[60:61]
	s_add_i32 m0, s57, 0x2000
	s_nop 0
	global_load_lds_dwordx4 v146, s[60:61]
	s_waitcnt vmcnt(6)
	s_barrier
	s_setprio 1
	v_mfma_scale_f32_16x16x128_f8f6f4 v[66:69], v[214:221], v[176:183], v[66:69], v174, v174 op_sel_hi:[0,0,0]
	v_mfma_scale_f32_16x16x128_f8f6f4 v[58:61], v[222:229], v[176:183], v[58:61], v174, v174 op_sel_hi:[0,0,0]
	v_mfma_scale_f32_16x16x128_f8f6f4 v[50:53], v[214:221], v[184:191], v[50:53], v174, v174 op_sel_hi:[0,0,0]
	v_mfma_scale_f32_16x16x128_f8f6f4 v[42:45], v[222:229], v[184:191], v[42:45], v174, v174 op_sel_hi:[0,0,0]
	v_mfma_scale_f32_16x16x128_f8f6f4 v[34:37], v[214:221], v[192:199], v[34:37], v174, v174 op_sel_hi:[0,0,0]
	v_mfma_scale_f32_16x16x128_f8f6f4 v[26:29], v[222:229], v[192:199], v[26:29], v174, v174 op_sel_hi:[0,0,0]
	v_mfma_scale_f32_16x16x128_f8f6f4 v[22:25], v[214:221], v[206:213], v[22:25], v174, v174 op_sel_hi:[0,0,0]
	v_mfma_scale_f32_16x16x128_f8f6f4 v[18:21], v[222:229], v[206:213], v[18:21], v174, v174 op_sel_hi:[0,0,0]
	s_setprio 0
	s_add_i32 s57, 0, 0x18000
	v_add_u32_e32 v14, s57, v170
	s_barrier
	ds_read_b128 v[2:5], v14
	ds_read_b128 v[6:9], v14 offset:1024
	ds_read_b128 v[10:13], v14 offset:2048
	ds_read_b128 v[14:17], v14 offset:3072
	s_add_u32 s36, s36, 0x40000
	s_addc_u32 s37, s37, 0
	s_mov_b32 m0, s42
	ds_read_b128 v[176:179], v173 offset:32768
	ds_read_b128 v[180:183], v173 offset:33792
	ds_read_b128 v[184:187], v173 offset:34816
	ds_read_b128 v[188:191], v173 offset:35840
	ds_read_b128 v[192:195], v173 offset:36864
	ds_read_b128 v[196:199], v173 offset:37888
	ds_read_b128 v[206:209], v173 offset:38912
	ds_read_b128 v[210:213], v173 offset:39936
	global_load_lds_dwordx4 v152, s[36:37]
	s_mov_b32 m0, s43
	s_nop 0
	global_load_lds_dwordx4 v148, s[36:37]
	s_waitcnt lgkmcnt(8)
	s_barrier
	s_waitcnt lgkmcnt(0)
	s_setprio 1
	s_waitcnt lgkmcnt(0)
	v_mfma_scale_f32_16x16x128_f8f6f4 v[142:145], v[2:9], v[176:183], v[142:145], v174, v174 op_sel_hi:[0,0,0]
	v_mfma_scale_f32_16x16x128_f8f6f4 v[138:141], v[10:17], v[176:183], v[138:141], v174, v174 op_sel_hi:[0,0,0]
	v_mfma_scale_f32_16x16x128_f8f6f4 v[134:137], v[2:9], v[184:191], v[134:137], v174, v174 op_sel_hi:[0,0,0]
	v_mfma_scale_f32_16x16x128_f8f6f4 v[126:129], v[10:17], v[184:191], v[126:129], v174, v174 op_sel_hi:[0,0,0]
	v_mfma_scale_f32_16x16x128_f8f6f4 v[118:121], v[2:9], v[192:199], v[118:121], v174, v174 op_sel_hi:[0,0,0]
	v_mfma_scale_f32_16x16x128_f8f6f4 v[110:113], v[10:17], v[192:199], v[110:113], v174, v174 op_sel_hi:[0,0,0]
	v_mfma_scale_f32_16x16x128_f8f6f4 v[102:105], v[2:9], v[206:213], v[102:105], v174, v174 op_sel_hi:[0,0,0]
	v_mfma_scale_f32_16x16x128_f8f6f4 v[94:97], v[10:17], v[206:213], v[94:97], v174, v174 op_sel_hi:[0,0,0]
	s_setprio 0
	s_barrier
	s_add_i32 s36, 0, 0x1c000
	s_add_i32 s37, s57, s38
	v_add_u32_e32 v200, s36, v170
	s_mov_b32 m0, s37
	ds_read_b128 v[214:217], v200
	ds_read_b128 v[218:221], v200 offset:1024
	ds_read_b128 v[222:225], v200 offset:2048
	ds_read_b128 v[226:229], v200 offset:3072
	global_load_lds_dwordx4 v150, s[66:67]
	s_add_i32 m0, s37, 0x2000
	s_nop 0
	global_load_lds_dwordx4 v146, s[66:67]
	s_barrier
	s_waitcnt lgkmcnt(0)
	s_setprio 1
	s_waitcnt lgkmcnt(0)
	v_mfma_scale_f32_16x16x128_f8f6f4 v[130:133], v[214:221], v[176:183], v[130:133], v174, v174 op_sel_hi:[0,0,0]
	v_mfma_scale_f32_16x16x128_f8f6f4 v[122:125], v[222:229], v[176:183], v[122:125], v174, v174 op_sel_hi:[0,0,0]
	v_mfma_scale_f32_16x16x128_f8f6f4 v[114:117], v[214:221], v[184:191], v[114:117], v174, v174 op_sel_hi:[0,0,0]
	v_mfma_scale_f32_16x16x128_f8f6f4 v[106:109], v[222:229], v[184:191], v[106:109], v174, v174 op_sel_hi:[0,0,0]
	v_mfma_scale_f32_16x16x128_f8f6f4 v[98:101], v[214:221], v[192:199], v[98:101], v174, v174 op_sel_hi:[0,0,0]
	v_mfma_scale_f32_16x16x128_f8f6f4 v[90:93], v[222:229], v[192:199], v[90:93], v174, v174 op_sel_hi:[0,0,0]
	v_mfma_scale_f32_16x16x128_f8f6f4 v[86:89], v[214:221], v[206:213], v[86:89], v174, v174 op_sel_hi:[0,0,0]
	v_mfma_scale_f32_16x16x128_f8f6f4 v[82:85], v[222:229], v[206:213], v[82:85], v174, v174 op_sel_hi:[0,0,0]
	s_setprio 0
	s_mov_b32 m0, s45
	s_barrier
	ds_read_b128 v[176:179], v173 offset:49152
	ds_read_b128 v[180:183], v173 offset:50176
	ds_read_b128 v[184:187], v173 offset:51200
	ds_read_b128 v[188:191], v173 offset:52224
	ds_read_b128 v[192:195], v173 offset:53248
	ds_read_b128 v[196:199], v173 offset:54272
	ds_read_b128 v[206:209], v173 offset:55296
	ds_read_b128 v[210:213], v173 offset:56320
	global_load_lds_dwordx4 v152, s[68:69]
	s_mov_b32 m0, s46
	s_nop 0
	global_load_lds_dwordx4 v148, s[68:69]
	s_barrier
	s_waitcnt lgkmcnt(0)
	s_setprio 1
	s_waitcnt lgkmcnt(0)
	v_mfma_scale_f32_16x16x128_f8f6f4 v[78:81], v[2:9], v[176:183], v[78:81], v174, v174 op_sel_hi:[0,0,0]
	v_mfma_scale_f32_16x16x128_f8f6f4 v[74:77], v[10:17], v[176:183], v[74:77], v174, v174 op_sel_hi:[0,0,0]
	v_mfma_scale_f32_16x16x128_f8f6f4 v[70:73], v[2:9], v[184:191], v[70:73], v174, v174 op_sel_hi:[0,0,0]
	v_mfma_scale_f32_16x16x128_f8f6f4 v[62:65], v[10:17], v[184:191], v[62:65], v174, v174 op_sel_hi:[0,0,0]
	v_mfma_scale_f32_16x16x128_f8f6f4 v[54:57], v[2:9], v[192:199], v[54:57], v174, v174 op_sel_hi:[0,0,0]
	v_mfma_scale_f32_16x16x128_f8f6f4 v[46:49], v[10:17], v[192:199], v[46:49], v174, v174 op_sel_hi:[0,0,0]
	v_mfma_scale_f32_16x16x128_f8f6f4 v[38:41], v[2:9], v[206:213], v[38:41], v174, v174 op_sel_hi:[0,0,0]
	v_mfma_scale_f32_16x16x128_f8f6f4 v[30:33], v[10:17], v[206:213], v[30:33], v174, v174 op_sel_hi:[0,0,0]
	s_setprio 0
	s_barrier
	s_add_u32 s34, s34, 0x40080
	s_addc_u32 s35, s35, 0
	s_add_i32 s36, s36, s38
	s_mov_b32 m0, s36
	s_nop 0
	global_load_lds_dwordx4 v150, s[34:35]
	s_add_i32 m0, s36, 0x2000
	s_nop 0
	global_load_lds_dwordx4 v146, s[34:35]
	s_waitcnt vmcnt(6)
	s_barrier
	s_setprio 1
	v_mfma_scale_f32_16x16x128_f8f6f4 v[66:69], v[214:221], v[176:183], v[66:69], v174, v174 op_sel_hi:[0,0,0]
	v_mfma_scale_f32_16x16x128_f8f6f4 v[58:61], v[222:229], v[176:183], v[58:61], v174, v174 op_sel_hi:[0,0,0]
	v_mfma_scale_f32_16x16x128_f8f6f4 v[50:53], v[214:221], v[184:191], v[50:53], v174, v174 op_sel_hi:[0,0,0]
	v_mfma_scale_f32_16x16x128_f8f6f4 v[42:45], v[222:229], v[184:191], v[42:45], v174, v174 op_sel_hi:[0,0,0]
	v_mfma_scale_f32_16x16x128_f8f6f4 v[34:37], v[214:221], v[192:199], v[34:37], v174, v174 op_sel_hi:[0,0,0]
	v_mfma_scale_f32_16x16x128_f8f6f4 v[26:29], v[222:229], v[192:199], v[26:29], v174, v174 op_sel_hi:[0,0,0]
	v_mfma_scale_f32_16x16x128_f8f6f4 v[22:25], v[214:221], v[206:213], v[22:25], v174, v174 op_sel_hi:[0,0,0]
	v_mfma_scale_f32_16x16x128_f8f6f4 v[18:21], v[222:229], v[206:213], v[18:21], v174, v174 op_sel_hi:[0,0,0]
	s_setprio 0
	s_add_i32 s56, s56, 2
	s_add_u32 s30, s30, 0x100
	s_addc_u32 s31, s31, 0
	s_add_u32 s54, s54, 0x100
	s_addc_u32 s55, s55, 0
	s_cmp_gt_u32 s56, 13
	s_barrier
	s_cbranch_scc0 .LBB0_202
	v_lshl_or_b32 v4, s51, 8, v171
	v_lshl_add_u32 v16, s28, 8, v1
	v_ashrrev_i32_e32 v5, 31, v4
	v_mov_b64_e32 v[2:3], s[96:97]
	v_mad_i64_i32 v[6:7], s[30:31], v16, s50, v[2:3]
	v_lshlrev_b64 v[4:5], 1, v[4:5]
	v_lshl_add_u64 v[10:11], v[6:7], 0, v[4:5]
	v_pk_mul_f32 v[8:9], v[144:145], s[8:9] op_sel_hi:[1,0]
	v_pk_mul_f32 v[6:7], v[142:143], s[8:9] op_sel_hi:[1,0]
	v_pk_mul_f32 v[12:13], v[140:141], s[8:9] op_sel_hi:[1,0]
	v_pk_mul_f32 v[14:15], v[138:139], s[8:9] op_sel_hi:[1,0]
	v_cvt_pk_bf16_f32 v6, v6, v7
	v_cvt_pk_bf16_f32 v7, v8, v9
	v_cvt_pk_bf16_f32 v8, v14, v15
	v_cvt_pk_bf16_f32 v9, v12, v13
	global_store_dwordx4 v[10:11], v[6:9], off
	v_pk_mul_f32 v[12:13], v[124:125], s[8:9] op_sel_hi:[1,0]
	v_pk_mul_f32 v[14:15], v[122:123], s[8:9] op_sel_hi:[1,0]
	v_pk_mul_f32 v[8:9], v[132:133], s[8:9] op_sel_hi:[1,0]
	v_pk_mul_f32 v[6:7], v[130:131], s[8:9] op_sel_hi:[1,0]
	s_and_b64 vcc, exec, s[0:1]
	v_cvt_pk_bf16_f32 v6, v6, v7
	v_cvt_pk_bf16_f32 v7, v8, v9
	v_cvt_pk_bf16_f32 v8, v14, v15
	v_cvt_pk_bf16_f32 v9, v12, v13
	global_store_dwordx4 v[10:11], v[6:9], off offset:256
	v_pk_mul_f32 v[12:13], v[128:129], s[8:9] op_sel_hi:[1,0]
	v_pk_mul_f32 v[14:15], v[126:127], s[8:9] op_sel_hi:[1,0]
	v_or_b32_e32 v6, 16, v16
	v_mad_i64_i32 v[6:7], s[30:31], v6, s50, v[2:3]
	v_lshl_add_u64 v[10:11], v[6:7], 0, v[4:5]
	v_pk_mul_f32 v[8:9], v[136:137], s[8:9] op_sel_hi:[1,0]
	v_pk_mul_f32 v[6:7], v[134:135], s[8:9] op_sel_hi:[1,0]
	s_mov_b32 s51, s10
	v_cvt_pk_bf16_f32 v6, v6, v7
	v_cvt_pk_bf16_f32 v7, v8, v9
	v_cvt_pk_bf16_f32 v8, v14, v15
	v_cvt_pk_bf16_f32 v9, v12, v13
	global_store_dwordx4 v[10:11], v[6:9], off
	v_pk_mul_f32 v[12:13], v[108:109], s[8:9] op_sel_hi:[1,0]
	v_pk_mul_f32 v[14:15], v[106:107], s[8:9] op_sel_hi:[1,0]
	v_pk_mul_f32 v[8:9], v[116:117], s[8:9] op_sel_hi:[1,0]
	v_pk_mul_f32 v[6:7], v[114:115], s[8:9] op_sel_hi:[1,0]
	s_mov_b32 s28, s20
	v_cvt_pk_bf16_f32 v6, v6, v7
	v_cvt_pk_bf16_f32 v7, v8, v9
	v_cvt_pk_bf16_f32 v8, v14, v15
	v_cvt_pk_bf16_f32 v9, v12, v13
	global_store_dwordx4 v[10:11], v[6:9], off offset:256
	v_pk_mul_f32 v[12:13], v[112:113], s[8:9] op_sel_hi:[1,0]
	v_pk_mul_f32 v[14:15], v[110:111], s[8:9] op_sel_hi:[1,0]
	v_or_b32_e32 v6, 32, v16
	v_mad_i64_i32 v[6:7], s[30:31], v6, s50, v[2:3]
	v_lshl_add_u64 v[10:11], v[6:7], 0, v[4:5]
	v_pk_mul_f32 v[8:9], v[120:121], s[8:9] op_sel_hi:[1,0]
	v_pk_mul_f32 v[6:7], v[118:119], s[8:9] op_sel_hi:[1,0]
	s_mov_b64 s[34:35], s[26:27]
	v_cvt_pk_bf16_f32 v6, v6, v7
	v_cvt_pk_bf16_f32 v7, v8, v9
	v_cvt_pk_bf16_f32 v8, v14, v15
	v_cvt_pk_bf16_f32 v9, v12, v13
	global_store_dwordx4 v[10:11], v[6:9], off
	v_pk_mul_f32 v[12:13], v[92:93], s[8:9] op_sel_hi:[1,0]
	v_pk_mul_f32 v[14:15], v[90:91], s[8:9] op_sel_hi:[1,0]
	v_pk_mul_f32 v[8:9], v[100:101], s[8:9] op_sel_hi:[1,0]
	v_pk_mul_f32 v[6:7], v[98:99], s[8:9] op_sel_hi:[1,0]
	s_nop 0
	v_cvt_pk_bf16_f32 v6, v6, v7
	v_cvt_pk_bf16_f32 v7, v8, v9
	v_cvt_pk_bf16_f32 v8, v14, v15
	v_cvt_pk_bf16_f32 v9, v12, v13
	global_store_dwordx4 v[10:11], v[6:9], off offset:256
	v_pk_mul_f32 v[12:13], v[96:97], s[8:9] op_sel_hi:[1,0]
	v_pk_mul_f32 v[14:15], v[94:95], s[8:9] op_sel_hi:[1,0]
	v_or_b32_e32 v6, 48, v16
	v_mad_i64_i32 v[6:7], s[30:31], v6, s50, v[2:3]
	v_lshl_add_u64 v[10:11], v[6:7], 0, v[4:5]
	v_pk_mul_f32 v[8:9], v[104:105], s[8:9] op_sel_hi:[1,0]
	v_pk_mul_f32 v[6:7], v[102:103], s[8:9] op_sel_hi:[1,0]
	s_nop 0
	v_cvt_pk_bf16_f32 v6, v6, v7
	v_cvt_pk_bf16_f32 v7, v8, v9
	v_cvt_pk_bf16_f32 v8, v14, v15
	v_cvt_pk_bf16_f32 v9, v12, v13
	global_store_dwordx4 v[10:11], v[6:9], off
	v_pk_mul_f32 v[12:13], v[84:85], s[8:9] op_sel_hi:[1,0]
	v_pk_mul_f32 v[14:15], v[82:83], s[8:9] op_sel_hi:[1,0]
	v_pk_mul_f32 v[8:9], v[88:89], s[8:9] op_sel_hi:[1,0]
	v_pk_mul_f32 v[6:7], v[86:87], s[8:9] op_sel_hi:[1,0]
	s_nop 0
	v_cvt_pk_bf16_f32 v6, v6, v7
	v_cvt_pk_bf16_f32 v7, v8, v9
	v_cvt_pk_bf16_f32 v8, v14, v15
	v_cvt_pk_bf16_f32 v9, v12, v13
	global_store_dwordx4 v[10:11], v[6:9], off offset:256
	v_pk_mul_f32 v[12:13], v[76:77], s[8:9] op_sel_hi:[1,0]
	v_pk_mul_f32 v[14:15], v[74:75], s[8:9] op_sel_hi:[1,0]
	v_add_u32_e32 v6, 0x80, v16
	v_mad_i64_i32 v[6:7], s[30:31], v6, s50, v[2:3]
	v_lshl_add_u64 v[10:11], v[6:7], 0, v[4:5]
	v_pk_mul_f32 v[8:9], v[80:81], s[8:9] op_sel_hi:[1,0]
	v_pk_mul_f32 v[6:7], v[78:79], s[8:9] op_sel_hi:[1,0]
	s_nop 0
	v_cvt_pk_bf16_f32 v6, v6, v7
	v_cvt_pk_bf16_f32 v7, v8, v9
	v_cvt_pk_bf16_f32 v8, v14, v15
	v_cvt_pk_bf16_f32 v9, v12, v13
	global_store_dwordx4 v[10:11], v[6:9], off
	v_pk_mul_f32 v[12:13], v[60:61], s[8:9] op_sel_hi:[1,0]
	v_pk_mul_f32 v[14:15], v[58:59], s[8:9] op_sel_hi:[1,0]
	v_pk_mul_f32 v[8:9], v[68:69], s[8:9] op_sel_hi:[1,0]
	v_pk_mul_f32 v[6:7], v[66:67], s[8:9] op_sel_hi:[1,0]
	s_nop 0
	v_cvt_pk_bf16_f32 v6, v6, v7
	v_cvt_pk_bf16_f32 v7, v8, v9
	v_cvt_pk_bf16_f32 v8, v14, v15
	v_cvt_pk_bf16_f32 v9, v12, v13
	global_store_dwordx4 v[10:11], v[6:9], off offset:256
	v_pk_mul_f32 v[12:13], v[64:65], s[8:9] op_sel_hi:[1,0]
	v_pk_mul_f32 v[14:15], v[62:63], s[8:9] op_sel_hi:[1,0]
	v_add_u32_e32 v6, 0x90, v16
	v_mad_i64_i32 v[6:7], s[30:31], v6, s50, v[2:3]
	v_lshl_add_u64 v[10:11], v[6:7], 0, v[4:5]
	v_pk_mul_f32 v[8:9], v[72:73], s[8:9] op_sel_hi:[1,0]
	v_pk_mul_f32 v[6:7], v[70:71], s[8:9] op_sel_hi:[1,0]
	s_nop 0
	v_cvt_pk_bf16_f32 v6, v6, v7
	v_cvt_pk_bf16_f32 v7, v8, v9
	v_cvt_pk_bf16_f32 v8, v14, v15
	v_cvt_pk_bf16_f32 v9, v12, v13
	global_store_dwordx4 v[10:11], v[6:9], off
	v_pk_mul_f32 v[12:13], v[44:45], s[8:9] op_sel_hi:[1,0]
	v_pk_mul_f32 v[14:15], v[42:43], s[8:9] op_sel_hi:[1,0]
	v_pk_mul_f32 v[8:9], v[52:53], s[8:9] op_sel_hi:[1,0]
	v_pk_mul_f32 v[6:7], v[50:51], s[8:9] op_sel_hi:[1,0]
	s_nop 0
	v_cvt_pk_bf16_f32 v6, v6, v7
	v_cvt_pk_bf16_f32 v7, v8, v9
	v_cvt_pk_bf16_f32 v8, v14, v15
	v_cvt_pk_bf16_f32 v9, v12, v13
	global_store_dwordx4 v[10:11], v[6:9], off offset:256
	v_pk_mul_f32 v[12:13], v[48:49], s[8:9] op_sel_hi:[1,0]
	v_pk_mul_f32 v[14:15], v[46:47], s[8:9] op_sel_hi:[1,0]
	v_add_u32_e32 v6, 0xa0, v16
	v_mad_i64_i32 v[6:7], s[30:31], v6, s50, v[2:3]
	v_lshl_add_u64 v[10:11], v[6:7], 0, v[4:5]
	v_pk_mul_f32 v[8:9], v[56:57], s[8:9] op_sel_hi:[1,0]
	v_pk_mul_f32 v[6:7], v[54:55], s[8:9] op_sel_hi:[1,0]
	s_nop 0
	v_cvt_pk_bf16_f32 v6, v6, v7
	v_cvt_pk_bf16_f32 v7, v8, v9
	v_cvt_pk_bf16_f32 v8, v14, v15
	v_cvt_pk_bf16_f32 v9, v12, v13
	global_store_dwordx4 v[10:11], v[6:9], off
	v_pk_mul_f32 v[12:13], v[28:29], s[8:9] op_sel_hi:[1,0]
	v_pk_mul_f32 v[14:15], v[26:27], s[8:9] op_sel_hi:[1,0]
	v_pk_mul_f32 v[8:9], v[36:37], s[8:9] op_sel_hi:[1,0]
	v_pk_mul_f32 v[6:7], v[34:35], s[8:9] op_sel_hi:[1,0]
	s_nop 0
	v_cvt_pk_bf16_f32 v6, v6, v7
	v_cvt_pk_bf16_f32 v7, v8, v9
	v_cvt_pk_bf16_f32 v8, v14, v15
	v_cvt_pk_bf16_f32 v9, v12, v13
	global_store_dwordx4 v[10:11], v[6:9], off offset:256
	v_pk_mul_f32 v[10:11], v[30:31], s[8:9] op_sel_hi:[1,0]
	s_nop 0
	v_add_u32_e32 v6, 0xb0, v16
	v_mad_i64_i32 v[2:3], s[30:31], v6, s50, v[2:3]
	v_lshl_add_u64 v[6:7], v[2:3], 0, v[4:5]
	v_pk_mul_f32 v[4:5], v[40:41], s[8:9] op_sel_hi:[1,0]
	v_pk_mul_f32 v[2:3], v[38:39], s[8:9] op_sel_hi:[1,0]
	v_pk_mul_f32 v[8:9], v[32:33], s[8:9] op_sel_hi:[1,0]
	v_cvt_pk_bf16_f32 v2, v2, v3
	v_cvt_pk_bf16_f32 v3, v4, v5
	v_cvt_pk_bf16_f32 v4, v10, v11
	v_cvt_pk_bf16_f32 v5, v8, v9
	global_store_dwordx4 v[6:7], v[2:5], off
	v_pk_mul_f32 v[8:9], v[20:21], s[8:9] op_sel_hi:[1,0]
	v_pk_mul_f32 v[10:11], v[18:19], s[8:9] op_sel_hi:[1,0]
	v_pk_mul_f32 v[4:5], v[24:25], s[8:9] op_sel_hi:[1,0]
	v_pk_mul_f32 v[2:3], v[22:23], s[8:9] op_sel_hi:[1,0]
	s_mov_b64 s[30:31], s[22:23]
	v_cvt_pk_bf16_f32 v2, v2, v3
	v_cvt_pk_bf16_f32 v3, v4, v5
	v_cvt_pk_bf16_f32 v4, v10, v11
	v_cvt_pk_bf16_f32 v5, v8, v9
	global_store_dwordx4 v[6:7], v[2:5], off offset:256
	s_cbranch_vccz .LBB0_199
	s_waitcnt vmcnt(0)
	s_cmpk_gt_u32 s2, 0xff
	s_cbranch_scc1 .LBB0_206
	s_barrier

.LBB0_620:
	ds_read_b128 v[152:155], v148
	ds_read_b128 v[156:159], v148 offset:1024
	ds_read_b128 v[160:163], v148 offset:2048
	ds_read_b128 v[164:167], v148 offset:3072
	s_add_u32 s30, s28, 0xfff80080
	s_addc_u32 s31, s29, -1
	s_cmp_eq_u32 s60, 28
	s_cselect_b32 s35, s21, s31
	s_cselect_b32 s34, s54, s30
	s_cselect_b32 s31, s19, s57
	s_cselect_b32 s30, s55, s56
	s_add_i32 m0, s17, 0xc000
	ds_read_b128 v[168:171], v149
	ds_read_b128 v[172:175], v149 offset:1024
	ds_read_b128 v[176:179], v149 offset:2048
	ds_read_b128 v[180:183], v149 offset:3072
	ds_read_b128 v[184:187], v149 offset:4096
	ds_read_b128 v[188:191], v149 offset:5120
	ds_read_b128 v[192:195], v149 offset:6144
	ds_read_b128 v[196:199], v149 offset:7168
	global_load_lds_dwordx4 v138, s[28:29]
	s_add_i32 m0, s17, 0xe000
	s_nop 0
	global_load_lds_dwordx4 v140, s[28:29]
	s_waitcnt lgkmcnt(8)
	s_barrier
	s_waitcnt lgkmcnt(0)
	s_setprio 1
	s_waitcnt lgkmcnt(0)
	v_mfma_f32_16x16x32_bf16 v[126:129], v[152:155], v[168:171], v[126:129]
	v_mfma_f32_16x16x32_bf16 v[122:125], v[160:163], v[168:171], v[122:125]
	v_mfma_f32_16x16x32_bf16 v[118:121], v[152:155], v[176:179], v[118:121]
	v_mfma_f32_16x16x32_bf16 v[114:117], v[160:163], v[176:179], v[114:117]
	v_mfma_f32_16x16x32_bf16 v[102:105], v[152:155], v[184:187], v[102:105]
	v_mfma_f32_16x16x32_bf16 v[98:101], v[160:163], v[184:187], v[98:101]
	v_mfma_f32_16x16x32_bf16 v[86:89], v[152:155], v[192:195], v[86:89]
	v_mfma_f32_16x16x32_bf16 v[82:85], v[160:163], v[192:195], v[82:85]
	v_mfma_f32_16x16x32_bf16 v[126:129], v[156:159], v[172:175], v[126:129]
	v_mfma_f32_16x16x32_bf16 v[122:125], v[164:167], v[172:175], v[122:125]
	v_mfma_f32_16x16x32_bf16 v[118:121], v[156:159], v[180:183], v[118:121]
	v_mfma_f32_16x16x32_bf16 v[114:117], v[164:167], v[180:183], v[114:117]
	v_mfma_f32_16x16x32_bf16 v[102:105], v[156:159], v[188:191], v[102:105]
	v_mfma_f32_16x16x32_bf16 v[98:101], v[164:167], v[188:191], v[98:101]
	v_mfma_f32_16x16x32_bf16 v[86:89], v[156:159], v[196:199], v[86:89]
	v_mfma_f32_16x16x32_bf16 v[82:85], v[164:167], v[196:199], v[82:85]
	s_setprio 0
	s_barrier
	s_add_i32 s61, s47, s37
	s_add_u32 s66, s30, 0x80
	s_addc_u32 s67, s31, 0
	s_mov_b32 m0, s61
	ds_read_b128 v[200:203], v150
	ds_read_b128 v[206:209], v150 offset:1024
	ds_read_b128 v[210:213], v150 offset:2048
	ds_read_b128 v[214:217], v150 offset:3072
	global_load_lds_dwordx4 v134, s[30:31]
	s_add_i32 m0, s61, 0x2000
	s_nop 0
	global_load_lds_dwordx4 v130, s[30:31]
	s_barrier
	s_waitcnt lgkmcnt(0)
	s_setprio 1
	s_waitcnt lgkmcnt(0)
	v_mfma_f32_16x16x32_bf16 v[110:113], v[200:203], v[168:171], v[110:113]
	v_mfma_f32_16x16x32_bf16 v[106:109], v[210:213], v[168:171], v[106:109]
	v_mfma_f32_16x16x32_bf16 v[94:97], v[200:203], v[176:179], v[94:97]
	v_mfma_f32_16x16x32_bf16 v[90:93], v[210:213], v[176:179], v[90:93]
	v_mfma_f32_16x16x32_bf16 v[78:81], v[200:203], v[184:187], v[78:81]
	v_mfma_f32_16x16x32_bf16 v[74:77], v[210:213], v[184:187], v[74:77]
	v_mfma_f32_16x16x32_bf16 v[70:73], v[200:203], v[192:195], v[70:73]
	v_mfma_f32_16x16x32_bf16 v[66:69], v[210:213], v[192:195], v[66:69]
	v_mfma_f32_16x16x32_bf16 v[110:113], v[206:209], v[172:175], v[110:113]
	v_mfma_f32_16x16x32_bf16 v[106:109], v[214:217], v[172:175], v[106:109]
	v_mfma_f32_16x16x32_bf16 v[94:97], v[206:209], v[180:183], v[94:97]
	v_mfma_f32_16x16x32_bf16 v[90:93], v[214:217], v[180:183], v[90:93]
	v_mfma_f32_16x16x32_bf16 v[78:81], v[206:209], v[188:191], v[78:81]
	v_mfma_f32_16x16x32_bf16 v[74:77], v[214:217], v[188:191], v[74:77]
	v_mfma_f32_16x16x32_bf16 v[70:73], v[206:209], v[196:199], v[70:73]
	v_mfma_f32_16x16x32_bf16 v[66:69], v[214:217], v[196:199], v[66:69]
	s_setprio 0
	s_mov_b32 m0, s17
	s_add_u32 s68, s34, 0x80
	s_addc_u32 s69, s35, 0
	s_barrier
	ds_read_b128 v[168:171], v149 offset:16384
	ds_read_b128 v[172:175], v149 offset:17408
	ds_read_b128 v[176:179], v149 offset:18432
	ds_read_b128 v[180:183], v149 offset:19456
	ds_read_b128 v[184:187], v149 offset:20480
	ds_read_b128 v[188:191], v149 offset:21504
	ds_read_b128 v[192:195], v149 offset:22528
	ds_read_b128 v[196:199], v149 offset:23552
	global_load_lds_dwordx4 v136, s[34:35]
	s_mov_b32 m0, s40
	s_nop 0
	global_load_lds_dwordx4 v132, s[34:35]
	s_barrier
	s_waitcnt lgkmcnt(0)
	s_setprio 1
	s_waitcnt lgkmcnt(0)
	v_mfma_f32_16x16x32_bf16 v[62:65], v[152:155], v[168:171], v[62:65]
	v_mfma_f32_16x16x32_bf16 v[58:61], v[160:163], v[168:171], v[58:61]
	v_mfma_f32_16x16x32_bf16 v[54:57], v[152:155], v[176:179], v[54:57]
	v_mfma_f32_16x16x32_bf16 v[50:53], v[160:163], v[176:179], v[50:53]
	v_mfma_f32_16x16x32_bf16 v[38:41], v[152:155], v[184:187], v[38:41]
	v_mfma_f32_16x16x32_bf16 v[34:37], v[160:163], v[184:187], v[34:37]
	v_mfma_f32_16x16x32_bf16 v[22:25], v[152:155], v[192:195], v[22:25]
	v_mfma_f32_16x16x32_bf16 v[18:21], v[160:163], v[192:195], v[18:21]
	v_mfma_f32_16x16x32_bf16 v[62:65], v[156:159], v[172:175], v[62:65]
	v_mfma_f32_16x16x32_bf16 v[58:61], v[164:167], v[172:175], v[58:61]
	v_mfma_f32_16x16x32_bf16 v[54:57], v[156:159], v[180:183], v[54:57]
	v_mfma_f32_16x16x32_bf16 v[50:53], v[164:167], v[180:183], v[50:53]
	v_mfma_f32_16x16x32_bf16 v[38:41], v[156:159], v[188:191], v[38:41]
	v_mfma_f32_16x16x32_bf16 v[34:37], v[164:167], v[188:191], v[34:37]
	v_mfma_f32_16x16x32_bf16 v[22:25], v[156:159], v[196:199], v[22:25]
	v_mfma_f32_16x16x32_bf16 v[18:21], v[164:167], v[196:199], v[18:21]
	s_setprio 0
	s_barrier
	s_add_u32 s62, s30, 0x80000
	s_addc_u32 s63, s31, 0
	s_add_i32 s61, s48, s37
	s_mov_b32 m0, s61
	s_nop 0
	global_load_lds_dwordx4 v134, s[62:63]
	s_add_i32 m0, s61, 0x2000
	s_nop 0
	global_load_lds_dwordx4 v130, s[62:63]
	s_waitcnt vmcnt(6)
	s_barrier
	s_setprio 1
	v_mfma_f32_16x16x32_bf16 v[46:49], v[200:203], v[168:171], v[46:49]
	v_mfma_f32_16x16x32_bf16 v[42:45], v[210:213], v[168:171], v[42:45]
	v_mfma_f32_16x16x32_bf16 v[30:33], v[200:203], v[176:179], v[30:33]
	v_mfma_f32_16x16x32_bf16 v[26:29], v[210:213], v[176:179], v[26:29]
	v_mfma_f32_16x16x32_bf16 v[14:17], v[200:203], v[184:187], v[14:17]
	v_mfma_f32_16x16x32_bf16 v[10:13], v[210:213], v[184:187], v[10:13]
	v_mfma_f32_16x16x32_bf16 v[6:9], v[200:203], v[192:195], v[6:9]
	v_mfma_f32_16x16x32_bf16 v[2:5], v[210:213], v[192:195], v[2:5]
	v_mfma_f32_16x16x32_bf16 v[46:49], v[206:209], v[172:175], v[46:49]
	v_mfma_f32_16x16x32_bf16 v[42:45], v[214:217], v[172:175], v[42:45]
	v_mfma_f32_16x16x32_bf16 v[30:33], v[206:209], v[180:183], v[30:33]
	v_mfma_f32_16x16x32_bf16 v[26:29], v[214:217], v[180:183], v[26:29]
	v_mfma_f32_16x16x32_bf16 v[14:17], v[206:209], v[188:191], v[14:17]
	v_mfma_f32_16x16x32_bf16 v[10:13], v[214:217], v[188:191], v[10:13]
	v_mfma_f32_16x16x32_bf16 v[6:9], v[206:209], v[196:199], v[6:9]
	v_mfma_f32_16x16x32_bf16 v[2:5], v[214:217], v[196:199], v[2:5]
	s_setprio 0
	s_add_i32 s61, 0, 0x18000
	v_add_u32_e32 v151, s61, v146
	s_barrier
	ds_read_b128 v[152:155], v151
	ds_read_b128 v[156:159], v151 offset:1024
	ds_read_b128 v[160:163], v151 offset:2048
	ds_read_b128 v[164:167], v151 offset:3072
	s_add_u32 s34, s34, 0x80000
	s_addc_u32 s35, s35, 0
	s_mov_b32 m0, s41
	ds_read_b128 v[168:171], v149 offset:32768
	ds_read_b128 v[172:175], v149 offset:33792
	ds_read_b128 v[176:179], v149 offset:34816
	ds_read_b128 v[180:183], v149 offset:35840
	ds_read_b128 v[184:187], v149 offset:36864
	ds_read_b128 v[188:191], v149 offset:37888
	ds_read_b128 v[192:195], v149 offset:38912
	ds_read_b128 v[196:199], v149 offset:39936
	global_load_lds_dwordx4 v136, s[34:35]
	s_mov_b32 m0, s42
	s_nop 0
	global_load_lds_dwordx4 v132, s[34:35]
	s_waitcnt lgkmcnt(8)
	s_barrier
	s_waitcnt lgkmcnt(0)
	s_setprio 1
	s_waitcnt lgkmcnt(0)
	v_mfma_f32_16x16x32_bf16 v[126:129], v[152:155], v[168:171], v[126:129]
	v_mfma_f32_16x16x32_bf16 v[122:125], v[160:163], v[168:171], v[122:125]
	v_mfma_f32_16x16x32_bf16 v[118:121], v[152:155], v[176:179], v[118:121]
	v_mfma_f32_16x16x32_bf16 v[114:117], v[160:163], v[176:179], v[114:117]
	v_mfma_f32_16x16x32_bf16 v[102:105], v[152:155], v[184:187], v[102:105]
	v_mfma_f32_16x16x32_bf16 v[98:101], v[160:163], v[184:187], v[98:101]
	v_mfma_f32_16x16x32_bf16 v[86:89], v[152:155], v[192:195], v[86:89]
	v_mfma_f32_16x16x32_bf16 v[82:85], v[160:163], v[192:195], v[82:85]
	v_mfma_f32_16x16x32_bf16 v[126:129], v[156:159], v[172:175], v[126:129]
	v_mfma_f32_16x16x32_bf16 v[122:125], v[164:167], v[172:175], v[122:125]
	v_mfma_f32_16x16x32_bf16 v[118:121], v[156:159], v[180:183], v[118:121]
	v_mfma_f32_16x16x32_bf16 v[114:117], v[164:167], v[180:183], v[114:117]
	v_mfma_f32_16x16x32_bf16 v[102:105], v[156:159], v[188:191], v[102:105]
	v_mfma_f32_16x16x32_bf16 v[98:101], v[164:167], v[188:191], v[98:101]
	v_mfma_f32_16x16x32_bf16 v[86:89], v[156:159], v[196:199], v[86:89]
	v_mfma_f32_16x16x32_bf16 v[82:85], v[164:167], v[196:199], v[82:85]
	s_setprio 0
	s_barrier
	s_add_i32 s34, 0, 0x1c000
	s_add_i32 s35, s61, s37
	v_add_u32_e32 v151, s34, v146
	s_mov_b32 m0, s35
	ds_read_b128 v[200:203], v151
	ds_read_b128 v[206:209], v151 offset:1024
	ds_read_b128 v[210:213], v151 offset:2048
	ds_read_b128 v[214:217], v151 offset:3072
	global_load_lds_dwordx4 v134, s[66:67]
	s_add_i32 m0, s35, 0x2000
	s_nop 0
	global_load_lds_dwordx4 v130, s[66:67]
	s_barrier
	s_waitcnt lgkmcnt(0)
	s_setprio 1
	s_waitcnt lgkmcnt(0)
	v_mfma_f32_16x16x32_bf16 v[110:113], v[200:203], v[168:171], v[110:113]
	v_mfma_f32_16x16x32_bf16 v[106:109], v[210:213], v[168:171], v[106:109]
	v_mfma_f32_16x16x32_bf16 v[94:97], v[200:203], v[176:179], v[94:97]
	v_mfma_f32_16x16x32_bf16 v[90:93], v[210:213], v[176:179], v[90:93]
	v_mfma_f32_16x16x32_bf16 v[78:81], v[200:203], v[184:187], v[78:81]
	v_mfma_f32_16x16x32_bf16 v[74:77], v[210:213], v[184:187], v[74:77]
	v_mfma_f32_16x16x32_bf16 v[70:73], v[200:203], v[192:195], v[70:73]
	v_mfma_f32_16x16x32_bf16 v[66:69], v[210:213], v[192:195], v[66:69]
	v_mfma_f32_16x16x32_bf16 v[110:113], v[206:209], v[172:175], v[110:113]
	v_mfma_f32_16x16x32_bf16 v[106:109], v[214:217], v[172:175], v[106:109]
	v_mfma_f32_16x16x32_bf16 v[94:97], v[206:209], v[180:183], v[94:97]
	v_mfma_f32_16x16x32_bf16 v[90:93], v[214:217], v[180:183], v[90:93]
	v_mfma_f32_16x16x32_bf16 v[78:81], v[206:209], v[188:191], v[78:81]
	v_mfma_f32_16x16x32_bf16 v[74:77], v[214:217], v[188:191], v[74:77]
	v_mfma_f32_16x16x32_bf16 v[70:73], v[206:209], v[196:199], v[70:73]
	v_mfma_f32_16x16x32_bf16 v[66:69], v[214:217], v[196:199], v[66:69]
	s_setprio 0
	s_mov_b32 m0, s44
	s_barrier
	ds_read_b128 v[168:171], v149 offset:49152
	ds_read_b128 v[172:175], v149 offset:50176
	ds_read_b128 v[176:179], v149 offset:51200
	ds_read_b128 v[180:183], v149 offset:52224
	ds_read_b128 v[184:187], v149 offset:53248
	ds_read_b128 v[188:191], v149 offset:54272
	ds_read_b128 v[192:195], v149 offset:55296
	ds_read_b128 v[196:199], v149 offset:56320
	global_load_lds_dwordx4 v136, s[68:69]
	s_mov_b32 m0, s45
	s_nop 0
	global_load_lds_dwordx4 v132, s[68:69]
	s_barrier
	s_waitcnt lgkmcnt(0)
	s_setprio 1
	s_waitcnt lgkmcnt(0)
	v_mfma_f32_16x16x32_bf16 v[62:65], v[152:155], v[168:171], v[62:65]
	v_mfma_f32_16x16x32_bf16 v[58:61], v[160:163], v[168:171], v[58:61]
	v_mfma_f32_16x16x32_bf16 v[54:57], v[152:155], v[176:179], v[54:57]
	v_mfma_f32_16x16x32_bf16 v[50:53], v[160:163], v[176:179], v[50:53]
	v_mfma_f32_16x16x32_bf16 v[38:41], v[152:155], v[184:187], v[38:41]
	v_mfma_f32_16x16x32_bf16 v[34:37], v[160:163], v[184:187], v[34:37]
	v_mfma_f32_16x16x32_bf16 v[22:25], v[152:155], v[192:195], v[22:25]
	v_mfma_f32_16x16x32_bf16 v[18:21], v[160:163], v[192:195], v[18:21]
	v_mfma_f32_16x16x32_bf16 v[62:65], v[156:159], v[172:175], v[62:65]
	v_mfma_f32_16x16x32_bf16 v[58:61], v[164:167], v[172:175], v[58:61]
	v_mfma_f32_16x16x32_bf16 v[54:57], v[156:159], v[180:183], v[54:57]
	v_mfma_f32_16x16x32_bf16 v[50:53], v[164:167], v[180:183], v[50:53]
	v_mfma_f32_16x16x32_bf16 v[38:41], v[156:159], v[188:191], v[38:41]
	v_mfma_f32_16x16x32_bf16 v[34:37], v[164:167], v[188:191], v[34:37]
	v_mfma_f32_16x16x32_bf16 v[22:25], v[156:159], v[196:199], v[22:25]
	v_mfma_f32_16x16x32_bf16 v[18:21], v[164:167], v[196:199], v[18:21]
	s_setprio 0
	s_barrier
	s_add_u32 s30, s30, 0x80080
	s_addc_u32 s31, s31, 0
	s_add_i32 s34, s34, s37
	s_mov_b32 m0, s34
	s_nop 0
	global_load_lds_dwordx4 v134, s[30:31]
	s_add_i32 m0, s34, 0x2000
	s_nop 0
	global_load_lds_dwordx4 v130, s[30:31]
	s_waitcnt vmcnt(6)
	s_barrier
	s_setprio 1
	v_mfma_f32_16x16x32_bf16 v[46:49], v[200:203], v[168:171], v[46:49]
	v_mfma_f32_16x16x32_bf16 v[42:45], v[210:213], v[168:171], v[42:45]
	v_mfma_f32_16x16x32_bf16 v[30:33], v[200:203], v[176:179], v[30:33]
	v_mfma_f32_16x16x32_bf16 v[26:29], v[210:213], v[176:179], v[26:29]
	v_mfma_f32_16x16x32_bf16 v[14:17], v[200:203], v[184:187], v[14:17]
	v_mfma_f32_16x16x32_bf16 v[10:13], v[210:213], v[184:187], v[10:13]
	v_mfma_f32_16x16x32_bf16 v[6:9], v[200:203], v[192:195], v[6:9]
	v_mfma_f32_16x16x32_bf16 v[2:5], v[210:213], v[192:195], v[2:5]
	v_mfma_f32_16x16x32_bf16 v[46:49], v[206:209], v[172:175], v[46:49]
	v_mfma_f32_16x16x32_bf16 v[42:45], v[214:217], v[172:175], v[42:45]
	v_mfma_f32_16x16x32_bf16 v[30:33], v[206:209], v[180:183], v[30:33]
	v_mfma_f32_16x16x32_bf16 v[26:29], v[214:217], v[180:183], v[26:29]
	v_mfma_f32_16x16x32_bf16 v[14:17], v[206:209], v[188:191], v[14:17]
	v_mfma_f32_16x16x32_bf16 v[10:13], v[214:217], v[188:191], v[10:13]
	v_mfma_f32_16x16x32_bf16 v[6:9], v[206:209], v[196:199], v[6:9]
	v_mfma_f32_16x16x32_bf16 v[2:5], v[214:217], v[196:199], v[2:5]
	s_setprio 0
	s_add_i32 s60, s60, 2
	s_add_u32 s28, s28, 0x100
	s_addc_u32 s29, s29, 0
	s_add_u32 s56, s56, 0x100
	s_addc_u32 s57, s57, 0
	s_cmp_gt_u32 s60, 29
	s_barrier
	s_cbranch_scc0 .LBB0_620
	v_lshl_add_u32 v152, s16, 8, v1
	v_lshl_or_b32 v154, s53, 8, v147
	v_ashrrev_i32_e32 v153, 31, v152
	v_ashrrev_i32_e32 v155, 31, v154
	v_lshlrev_b64 v[156:157], 12, v[152:153]
	v_lshl_add_u64 v[156:157], s[96:97], 0, v[156:157]
	v_lshlrev_b64 v[154:155], 1, v[154:155]
	v_lshl_add_u64 v[156:157], v[156:157], 0, v[154:155]
	v_cvt_pk_bf16_f32 v62, v62, v63
	v_cvt_pk_bf16_f32 v63, v64, v65
	v_cvt_pk_bf16_f32 v64, v58, v59
	v_add_co_u32_e32 v58, vcc, s49, v156
	v_cvt_pk_bf16_f32 v70, v70, v71
	v_cvt_pk_bf16_f32 v71, v72, v73
	v_cvt_pk_bf16_f32 v72, v66, v67
	v_lshl_add_u64 v[66:67], v[156:157], 0, s[6:7]
	v_addc_co_u32_e32 v59, vcc, 0, v157, vcc
	v_cvt_pk_bf16_f32 v46, v46, v47
	v_cvt_pk_bf16_f32 v47, v48, v49
	v_cvt_pk_bf16_f32 v48, v42, v43
	v_cvt_pk_bf16_f32 v49, v44, v45
	v_cvt_pk_bf16_f32 v110, v110, v111
	v_cvt_pk_bf16_f32 v111, v112, v113
	v_cvt_pk_bf16_f32 v112, v106, v107
	v_or_b32_e32 v106, 16, v152
	global_store_dwordx4 v[66:67], v[46:49], off offset:256
	v_ashrrev_i32_e32 v107, 31, v106
	v_cvt_pk_bf16_f32 v94, v94, v95
	v_add_co_u32_e32 v48, vcc, s50, v156
	v_cvt_pk_bf16_f32 v95, v96, v97
	v_cvt_pk_bf16_f32 v96, v90, v91
	v_or_b32_e32 v90, 32, v152
	v_lshl_add_u64 v[46:47], v[156:157], 0, s[10:11]
	v_addc_co_u32_e32 v49, vcc, 0, v157, vcc
	v_cvt_pk_bf16_f32 v30, v30, v31
	v_cvt_pk_bf16_f32 v31, v32, v33
	v_cvt_pk_bf16_f32 v32, v26, v27
	v_cvt_pk_bf16_f32 v33, v28, v29
	v_lshlrev_b64 v[106:107], 12, v[106:107]
	v_ashrrev_i32_e32 v91, 31, v90
	v_cvt_pk_bf16_f32 v78, v78, v79
	v_cvt_pk_bf16_f32 v79, v80, v81
	v_cvt_pk_bf16_f32 v80, v74, v75
	v_or_b32_e32 v74, 48, v152
	global_store_dwordx4 v[46:47], v[30:33], off offset:256
	v_cvt_pk_bf16_f32 v113, v108, v109
	v_lshl_add_u64 v[106:107], s[96:97], 0, v[106:107]
	v_add_co_u32_e32 v32, vcc, s51, v156
	v_lshlrev_b64 v[90:91], 12, v[90:91]
	v_ashrrev_i32_e32 v75, 31, v74
	v_lshl_add_u64 v[30:31], v[156:157], 0, s[12:13]
	v_addc_co_u32_e32 v33, vcc, 0, v157, vcc
	v_cvt_pk_bf16_f32 v14, v14, v15
	v_cvt_pk_bf16_f32 v15, v16, v17
	v_cvt_pk_bf16_f32 v16, v10, v11
	v_cvt_pk_bf16_f32 v17, v12, v13
	global_store_dwordx4 v[156:157], v[110:113], off offset:256
	v_cvt_pk_bf16_f32 v97, v92, v93
	v_lshl_add_u64 v[90:91], s[96:97], 0, v[90:91]
	v_lshl_add_u64 v[110:111], v[106:107], 0, v[154:155]
	v_lshlrev_b64 v[74:75], 12, v[74:75]
	global_store_dwordx4 v[30:31], v[14:17], off offset:256
	global_store_dwordx4 v[110:111], v[94:97], off offset:256
	v_cvt_pk_bf16_f32 v81, v76, v77
	v_add_co_u32_e32 v16, vcc, s52, v156
	v_lshl_add_u64 v[94:95], v[90:91], 0, v[154:155]
	v_lshl_add_u64 v[74:75], s[96:97], 0, v[74:75]
	v_addc_co_u32_e32 v17, vcc, 0, v157, vcc
	v_cvt_pk_bf16_f32 v126, v126, v127
	v_cvt_pk_bf16_f32 v127, v128, v129
	v_cvt_pk_bf16_f32 v128, v122, v123
	v_cvt_pk_bf16_f32 v129, v124, v125
	v_cvt_pk_bf16_f32 v106, v118, v119
	v_cvt_pk_bf16_f32 v107, v120, v121
	v_cvt_pk_bf16_f32 v108, v114, v115
	v_cvt_pk_bf16_f32 v109, v116, v117
	v_cvt_pk_bf16_f32 v90, v102, v103
	v_cvt_pk_bf16_f32 v91, v104, v105
	v_cvt_pk_bf16_f32 v92, v98, v99
	v_cvt_pk_bf16_f32 v93, v100, v101
	global_store_dwordx4 v[94:95], v[78:81], off offset:256
	v_cvt_pk_bf16_f32 v76, v82, v83
	v_cvt_pk_bf16_f32 v77, v84, v85
	v_lshl_add_u64 v[78:79], v[74:75], 0, v[154:155]
	v_cvt_pk_bf16_f32 v74, v86, v87
	v_cvt_pk_bf16_f32 v75, v88, v89
	v_cvt_pk_bf16_f32 v73, v68, v69
	v_cvt_pk_bf16_f32 v65, v60, v61
	v_cvt_pk_bf16_f32 v42, v54, v55
	v_cvt_pk_bf16_f32 v43, v56, v57
	v_cvt_pk_bf16_f32 v44, v50, v51
	v_cvt_pk_bf16_f32 v45, v52, v53
	v_cvt_pk_bf16_f32 v26, v38, v39
	v_cvt_pk_bf16_f32 v27, v40, v41
	v_cvt_pk_bf16_f32 v28, v34, v35
	v_cvt_pk_bf16_f32 v29, v36, v37
	v_lshl_add_u64 v[14:15], v[156:157], 0, s[14:15]
	v_cvt_pk_bf16_f32 v10, v22, v23
	v_cvt_pk_bf16_f32 v11, v24, v25
	v_cvt_pk_bf16_f32 v12, v18, v19
	v_cvt_pk_bf16_f32 v13, v20, v21
	v_cvt_pk_bf16_f32 v6, v6, v7
	v_cvt_pk_bf16_f32 v7, v8, v9
	v_cvt_pk_bf16_f32 v8, v2, v3
	v_cvt_pk_bf16_f32 v9, v4, v5
	s_and_b64 vcc, exec, s[0:1]
	s_mov_b32 s53, s18
	s_mov_b32 s16, s20
	s_mov_b64 s[30:31], s[26:27]
	s_mov_b64 s[28:29], s[22:23]
	global_store_dwordx4 v[156:157], v[126:129], off
	global_store_dwordx4 v[110:111], v[106:109], off
	global_store_dwordx4 v[94:95], v[90:93], off
	global_store_dwordx4 v[78:79], v[74:77], off
	global_store_dwordx4 v[78:79], v[70:73], off offset:256
	global_store_dwordx4 v[58:59], v[62:65], off
	global_store_dwordx4 v[48:49], v[42:45], off
	global_store_dwordx4 v[32:33], v[26:29], off
	global_store_dwordx4 v[16:17], v[10:13], off
	global_store_dwordx4 v[14:15], v[6:9], off offset:256
	s_cbranch_vccz .LBB0_617
	s_waitcnt vmcnt(0)
	s_cmpk_gt_u32 s2, 0xff
	s_cbranch_scc1 .LBB0_624
	s_barrier

.LBB0_820:
	ds_read_b128 v[2:5], v176
	ds_read_b128 v[6:9], v176 offset:1024
	ds_read_b128 v[10:13], v176 offset:2048
	ds_read_b128 v[14:17], v176 offset:3072
	s_add_u32 s26, s24, 0xfffc0080
	s_addc_u32 s27, s25, -1
	s_cmp_eq_u32 s60, 12
	s_cselect_b32 s29, s17, s27
	s_cselect_b32 s28, s23, s26
	s_cselect_b32 s27, s15, s59
	s_cselect_b32 s26, s56, s57
	s_add_i32 m0, s36, 0xc000
	ds_read_b128 v[190:193], v177
	ds_read_b128 v[194:197], v177 offset:1024
	ds_read_b128 v[214:217], v177 offset:2048
	ds_read_b128 v[218:221], v177 offset:3072
	ds_read_b128 v[222:225], v177 offset:4096
	ds_read_b128 v[226:229], v177 offset:5120
	ds_read_b128 v[230:233], v177 offset:6144
	ds_read_b128 v[234:237], v177 offset:7168
	global_load_lds_dwordx4 v158, s[24:25]
	s_add_i32 m0, s36, 0xe000
	s_nop 0
	global_load_lds_dwordx4 v160, s[24:25]
	s_waitcnt lgkmcnt(8)
	s_barrier
	s_waitcnt lgkmcnt(0)
	s_setprio 1
	s_waitcnt lgkmcnt(0)
	v_mfma_scale_f32_16x16x128_f8f6f4 v[142:145], v[2:9], v[190:197], v[142:145], v178, v178 op_sel_hi:[0,0,0]
	v_mfma_scale_f32_16x16x128_f8f6f4 v[138:141], v[10:17], v[190:197], v[138:141], v178, v178 op_sel_hi:[0,0,0]
	v_mfma_scale_f32_16x16x128_f8f6f4 v[126:129], v[2:9], v[214:221], v[126:129], v178, v178 op_sel_hi:[0,0,0]
	v_mfma_scale_f32_16x16x128_f8f6f4 v[122:125], v[10:17], v[214:221], v[122:125], v178, v178 op_sel_hi:[0,0,0]
	v_mfma_scale_f32_16x16x128_f8f6f4 v[110:113], v[2:9], v[222:229], v[110:113], v178, v178 op_sel_hi:[0,0,0]
	v_mfma_scale_f32_16x16x128_f8f6f4 v[106:109], v[10:17], v[222:229], v[106:109], v178, v178 op_sel_hi:[0,0,0]
	v_mfma_scale_f32_16x16x128_f8f6f4 v[94:97], v[2:9], v[230:237], v[94:97], v178, v178 op_sel_hi:[0,0,0]
	v_mfma_scale_f32_16x16x128_f8f6f4 v[90:93], v[10:17], v[230:237], v[90:93], v178, v178 op_sel_hi:[0,0,0]
	s_setprio 0
	s_barrier
	s_add_i32 s61, s48, s33
	s_add_u32 s66, s26, 0x80
	s_addc_u32 s67, s27, 0
	s_mov_b32 m0, s61
	ds_read_b128 v[238:241], v179
	ds_read_b128 v[242:245], v179 offset:1024
	ds_read_b128 v[246:249], v179 offset:2048
	ds_read_b128 v[250:253], v179 offset:3072
	global_load_lds_dwordx4 v150, s[26:27]
	s_add_i32 m0, s61, 0x2000
	s_nop 0
	global_load_lds_dwordx4 v146, s[26:27]
	s_barrier
	s_waitcnt lgkmcnt(0)
	s_setprio 1
	s_waitcnt lgkmcnt(0)
	v_mfma_scale_f32_16x16x128_f8f6f4 v[134:137], v[238:245], v[190:197], v[134:137], v178, v178 op_sel_hi:[0,0,0]
	v_mfma_scale_f32_16x16x128_f8f6f4 v[130:133], v[246:253], v[190:197], v[130:133], v178, v178 op_sel_hi:[0,0,0]
	v_mfma_scale_f32_16x16x128_f8f6f4 v[118:121], v[238:245], v[214:221], v[118:121], v178, v178 op_sel_hi:[0,0,0]
	v_mfma_scale_f32_16x16x128_f8f6f4 v[114:117], v[246:253], v[214:221], v[114:117], v178, v178 op_sel_hi:[0,0,0]
	v_mfma_scale_f32_16x16x128_f8f6f4 v[102:105], v[238:245], v[222:229], v[102:105], v178, v178 op_sel_hi:[0,0,0]
	v_mfma_scale_f32_16x16x128_f8f6f4 v[98:101], v[246:253], v[222:229], v[98:101], v178, v178 op_sel_hi:[0,0,0]
	v_mfma_scale_f32_16x16x128_f8f6f4 v[86:89], v[238:245], v[230:237], v[86:89], v178, v178 op_sel_hi:[0,0,0]
	v_mfma_scale_f32_16x16x128_f8f6f4 v[82:85], v[246:253], v[230:237], v[82:85], v178, v178 op_sel_hi:[0,0,0]
	s_setprio 0
	s_mov_b32 m0, s36
	s_add_u32 s68, s28, 0x80
	s_addc_u32 s69, s29, 0
	s_barrier
	ds_read_b128 v[190:193], v177 offset:16384
	ds_read_b128 v[194:197], v177 offset:17408
	ds_read_b128 v[214:217], v177 offset:18432
	ds_read_b128 v[218:221], v177 offset:19456
	ds_read_b128 v[222:225], v177 offset:20480
	ds_read_b128 v[226:229], v177 offset:21504
	ds_read_b128 v[230:233], v177 offset:22528
	ds_read_b128 v[234:237], v177 offset:23552
	global_load_lds_dwordx4 v152, s[28:29]
	s_mov_b32 m0, s37
	s_nop 0
	global_load_lds_dwordx4 v148, s[28:29]
	s_barrier
	s_waitcnt lgkmcnt(0)
	s_setprio 1
	s_waitcnt lgkmcnt(0)
	v_mfma_scale_f32_16x16x128_f8f6f4 v[78:81], v[2:9], v[190:197], v[78:81], v178, v178 op_sel_hi:[0,0,0]
	v_mfma_scale_f32_16x16x128_f8f6f4 v[74:77], v[10:17], v[190:197], v[74:77], v178, v178 op_sel_hi:[0,0,0]
	v_mfma_scale_f32_16x16x128_f8f6f4 v[62:65], v[2:9], v[214:221], v[62:65], v178, v178 op_sel_hi:[0,0,0]
	v_mfma_scale_f32_16x16x128_f8f6f4 v[58:61], v[10:17], v[214:221], v[58:61], v178, v178 op_sel_hi:[0,0,0]
	v_mfma_scale_f32_16x16x128_f8f6f4 v[50:53], v[2:9], v[222:229], v[50:53], v178, v178 op_sel_hi:[0,0,0]
	v_mfma_scale_f32_16x16x128_f8f6f4 v[42:45], v[10:17], v[222:229], v[42:45], v178, v178 op_sel_hi:[0,0,0]
	v_mfma_scale_f32_16x16x128_f8f6f4 v[34:37], v[2:9], v[230:237], v[34:37], v178, v178 op_sel_hi:[0,0,0]
	v_mfma_scale_f32_16x16x128_f8f6f4 v[26:29], v[10:17], v[230:237], v[26:29], v178, v178 op_sel_hi:[0,0,0]
	s_setprio 0
	s_barrier
	s_add_u32 s62, s26, 0x40000
	s_addc_u32 s63, s27, 0
	s_add_i32 s61, s49, s33
	s_mov_b32 m0, s61
	s_nop 0
	global_load_lds_dwordx4 v150, s[62:63]
	s_add_i32 m0, s61, 0x2000
	s_nop 0
	global_load_lds_dwordx4 v146, s[62:63]
	s_waitcnt vmcnt(6)
	s_barrier
	s_setprio 1
	v_mfma_scale_f32_16x16x128_f8f6f4 v[70:73], v[238:245], v[190:197], v[70:73], v178, v178 op_sel_hi:[0,0,0]
	v_mfma_scale_f32_16x16x128_f8f6f4 v[66:69], v[246:253], v[190:197], v[66:69], v178, v178 op_sel_hi:[0,0,0]
	v_mfma_scale_f32_16x16x128_f8f6f4 v[54:57], v[238:245], v[214:221], v[54:57], v178, v178 op_sel_hi:[0,0,0]
	v_mfma_scale_f32_16x16x128_f8f6f4 v[46:49], v[246:253], v[214:221], v[46:49], v178, v178 op_sel_hi:[0,0,0]
	v_mfma_scale_f32_16x16x128_f8f6f4 v[38:41], v[238:245], v[222:229], v[38:41], v178, v178 op_sel_hi:[0,0,0]
	v_mfma_scale_f32_16x16x128_f8f6f4 v[30:33], v[246:253], v[222:229], v[30:33], v178, v178 op_sel_hi:[0,0,0]
	v_mfma_scale_f32_16x16x128_f8f6f4 v[22:25], v[238:245], v[230:237], v[22:25], v178, v178 op_sel_hi:[0,0,0]
	v_mfma_scale_f32_16x16x128_f8f6f4 v[18:21], v[246:253], v[230:237], v[18:21], v178, v178 op_sel_hi:[0,0,0]
	s_setprio 0
	s_add_i32 s61, 0, 0x18000
	v_add_u32_e32 v14, s61, v175
	s_barrier
	ds_read_b128 v[2:5], v14
	ds_read_b128 v[6:9], v14 offset:1024
	ds_read_b128 v[10:13], v14 offset:2048
	ds_read_b128 v[14:17], v14 offset:3072
	s_add_u32 s28, s28, 0x40000
	s_addc_u32 s29, s29, 0
	s_mov_b32 m0, s38
	ds_read_b128 v[190:193], v177 offset:32768
	ds_read_b128 v[194:197], v177 offset:33792
	ds_read_b128 v[214:217], v177 offset:34816
	ds_read_b128 v[218:221], v177 offset:35840
	ds_read_b128 v[222:225], v177 offset:36864
	ds_read_b128 v[226:229], v177 offset:37888
	ds_read_b128 v[230:233], v177 offset:38912
	ds_read_b128 v[234:237], v177 offset:39936
	global_load_lds_dwordx4 v152, s[28:29]
	s_mov_b32 m0, s39
	s_nop 0
	global_load_lds_dwordx4 v148, s[28:29]
	s_waitcnt lgkmcnt(8)
	s_barrier
	s_waitcnt lgkmcnt(0)
	s_setprio 1
	s_waitcnt lgkmcnt(0)
	v_mfma_scale_f32_16x16x128_f8f6f4 v[142:145], v[2:9], v[190:197], v[142:145], v178, v178 op_sel_hi:[0,0,0]
	v_mfma_scale_f32_16x16x128_f8f6f4 v[138:141], v[10:17], v[190:197], v[138:141], v178, v178 op_sel_hi:[0,0,0]
	v_mfma_scale_f32_16x16x128_f8f6f4 v[126:129], v[2:9], v[214:221], v[126:129], v178, v178 op_sel_hi:[0,0,0]
	v_mfma_scale_f32_16x16x128_f8f6f4 v[122:125], v[10:17], v[214:221], v[122:125], v178, v178 op_sel_hi:[0,0,0]
	v_mfma_scale_f32_16x16x128_f8f6f4 v[110:113], v[2:9], v[222:229], v[110:113], v178, v178 op_sel_hi:[0,0,0]
	v_mfma_scale_f32_16x16x128_f8f6f4 v[106:109], v[10:17], v[222:229], v[106:109], v178, v178 op_sel_hi:[0,0,0]
	v_mfma_scale_f32_16x16x128_f8f6f4 v[94:97], v[2:9], v[230:237], v[94:97], v178, v178 op_sel_hi:[0,0,0]
	v_mfma_scale_f32_16x16x128_f8f6f4 v[90:93], v[10:17], v[230:237], v[90:93], v178, v178 op_sel_hi:[0,0,0]
	s_setprio 0
	s_barrier
	s_add_i32 s28, 0, 0x1c000
	s_add_i32 s29, s61, s33
	v_add_u32_e32 v154, s28, v175
	s_mov_b32 m0, s29
	ds_read_b128 v[238:241], v154
	ds_read_b128 v[242:245], v154 offset:1024
	ds_read_b128 v[246:249], v154 offset:2048
	ds_read_b128 v[250:253], v154 offset:3072
	global_load_lds_dwordx4 v150, s[66:67]
	s_add_i32 m0, s29, 0x2000
	s_nop 0
	global_load_lds_dwordx4 v146, s[66:67]
	s_barrier
	s_waitcnt lgkmcnt(0)
	s_setprio 1
	s_waitcnt lgkmcnt(0)
	v_mfma_scale_f32_16x16x128_f8f6f4 v[134:137], v[238:245], v[190:197], v[134:137], v178, v178 op_sel_hi:[0,0,0]
	v_mfma_scale_f32_16x16x128_f8f6f4 v[130:133], v[246:253], v[190:197], v[130:133], v178, v178 op_sel_hi:[0,0,0]
	v_mfma_scale_f32_16x16x128_f8f6f4 v[118:121], v[238:245], v[214:221], v[118:121], v178, v178 op_sel_hi:[0,0,0]
	v_mfma_scale_f32_16x16x128_f8f6f4 v[114:117], v[246:253], v[214:221], v[114:117], v178, v178 op_sel_hi:[0,0,0]
	v_mfma_scale_f32_16x16x128_f8f6f4 v[102:105], v[238:245], v[222:229], v[102:105], v178, v178 op_sel_hi:[0,0,0]
	v_mfma_scale_f32_16x16x128_f8f6f4 v[98:101], v[246:253], v[222:229], v[98:101], v178, v178 op_sel_hi:[0,0,0]
	v_mfma_scale_f32_16x16x128_f8f6f4 v[86:89], v[238:245], v[230:237], v[86:89], v178, v178 op_sel_hi:[0,0,0]
	v_mfma_scale_f32_16x16x128_f8f6f4 v[82:85], v[246:253], v[230:237], v[82:85], v178, v178 op_sel_hi:[0,0,0]
	s_setprio 0
	s_mov_b32 m0, s45
	s_barrier
	ds_read_b128 v[190:193], v177 offset:49152
	ds_read_b128 v[194:197], v177 offset:50176
	ds_read_b128 v[214:217], v177 offset:51200
	ds_read_b128 v[218:221], v177 offset:52224
	ds_read_b128 v[222:225], v177 offset:53248
	ds_read_b128 v[226:229], v177 offset:54272
	ds_read_b128 v[230:233], v177 offset:55296
	ds_read_b128 v[234:237], v177 offset:56320
	global_load_lds_dwordx4 v152, s[68:69]
	s_mov_b32 m0, s46
	s_nop 0
	global_load_lds_dwordx4 v148, s[68:69]
	s_barrier
	s_waitcnt lgkmcnt(0)
	s_setprio 1
	s_waitcnt lgkmcnt(0)
	v_mfma_scale_f32_16x16x128_f8f6f4 v[78:81], v[2:9], v[190:197], v[78:81], v178, v178 op_sel_hi:[0,0,0]
	v_mfma_scale_f32_16x16x128_f8f6f4 v[74:77], v[10:17], v[190:197], v[74:77], v178, v178 op_sel_hi:[0,0,0]
	v_mfma_scale_f32_16x16x128_f8f6f4 v[62:65], v[2:9], v[214:221], v[62:65], v178, v178 op_sel_hi:[0,0,0]
	v_mfma_scale_f32_16x16x128_f8f6f4 v[58:61], v[10:17], v[214:221], v[58:61], v178, v178 op_sel_hi:[0,0,0]
	v_mfma_scale_f32_16x16x128_f8f6f4 v[50:53], v[2:9], v[222:229], v[50:53], v178, v178 op_sel_hi:[0,0,0]
	v_mfma_scale_f32_16x16x128_f8f6f4 v[42:45], v[10:17], v[222:229], v[42:45], v178, v178 op_sel_hi:[0,0,0]
	v_mfma_scale_f32_16x16x128_f8f6f4 v[34:37], v[2:9], v[230:237], v[34:37], v178, v178 op_sel_hi:[0,0,0]
	v_mfma_scale_f32_16x16x128_f8f6f4 v[26:29], v[10:17], v[230:237], v[26:29], v178, v178 op_sel_hi:[0,0,0]
	s_setprio 0
	s_barrier
	s_add_u32 s26, s26, 0x40080
	s_addc_u32 s27, s27, 0
	s_add_i32 s28, s28, s33
	s_mov_b32 m0, s28
	s_nop 0
	global_load_lds_dwordx4 v150, s[26:27]
	s_add_i32 m0, s28, 0x2000
	s_nop 0
	global_load_lds_dwordx4 v146, s[26:27]
	s_waitcnt vmcnt(6)
	s_barrier
	s_setprio 1
	v_mfma_scale_f32_16x16x128_f8f6f4 v[70:73], v[238:245], v[190:197], v[70:73], v178, v178 op_sel_hi:[0,0,0]
	v_mfma_scale_f32_16x16x128_f8f6f4 v[66:69], v[246:253], v[190:197], v[66:69], v178, v178 op_sel_hi:[0,0,0]
	v_mfma_scale_f32_16x16x128_f8f6f4 v[54:57], v[238:245], v[214:221], v[54:57], v178, v178 op_sel_hi:[0,0,0]
	v_mfma_scale_f32_16x16x128_f8f6f4 v[46:49], v[246:253], v[214:221], v[46:49], v178, v178 op_sel_hi:[0,0,0]
	v_mfma_scale_f32_16x16x128_f8f6f4 v[38:41], v[238:245], v[222:229], v[38:41], v178, v178 op_sel_hi:[0,0,0]
	v_mfma_scale_f32_16x16x128_f8f6f4 v[30:33], v[246:253], v[222:229], v[30:33], v178, v178 op_sel_hi:[0,0,0]
	v_mfma_scale_f32_16x16x128_f8f6f4 v[22:25], v[238:245], v[230:237], v[22:25], v178, v178 op_sel_hi:[0,0,0]
	v_mfma_scale_f32_16x16x128_f8f6f4 v[18:21], v[246:253], v[230:237], v[18:21], v178, v178 op_sel_hi:[0,0,0]
	s_setprio 0
	s_add_i32 s60, s60, 2
	s_add_u32 s24, s24, 0x100
	s_addc_u32 s25, s25, 0
	s_add_u32 s57, s57, 0x100
	s_addc_u32 s59, s59, 0
	s_cmp_gt_u32 s60, 13
	s_barrier
	s_cbranch_scc0 .LBB0_820
	v_lshl_add_u32 v10, s22, 8, v174
	s_add_i32 s15, s55, -4
	s_mov_b64 s[22:23], -1
	s_cmp_lt_u32 s15, 8
	v_or_b32_e32 v8, 16, v10
	v_or_b32_e32 v4, 32, v10
	v_or_b32_e32 v2, 48, v10
	s_cbranch_scc1 .LBB0_823
	s_lshl_b32 s22, s55, 8
	s_ashr_i32 s23, s22, 31
	v_mov_b64_e32 v[6:7], s[96:97]
	v_mad_i64_i32 v[12:13], s[24:25], v10, s50, v[6:7]
	s_lshl_b64 s[22:23], s[22:23], 1
	v_lshl_add_u64 v[12:13], v[12:13], 0, s[22:23]
	v_lshlrev_b32_e32 v154, 1, v156
	v_lshl_add_u64 v[16:17], v[12:13], 0, v[154:155]
	v_pk_mul_f32 v[14:15], v[144:145], s[8:9] op_sel_hi:[1,0]
	v_pk_mul_f32 v[12:13], v[142:143], s[8:9] op_sel_hi:[1,0]
	v_pk_mul_f32 v[166:167], v[140:141], s[8:9] op_sel_hi:[1,0]
	v_pk_mul_f32 v[168:169], v[138:139], s[8:9] op_sel_hi:[1,0]
	v_cvt_pk_bf16_f32 v12, v12, v13
	v_cvt_pk_bf16_f32 v13, v14, v15
	v_cvt_pk_bf16_f32 v14, v168, v169
	v_cvt_pk_bf16_f32 v15, v166, v167
	global_store_dwordx4 v[16:17], v[12:15], off
	v_pk_mul_f32 v[166:167], v[132:133], s[8:9] op_sel_hi:[1,0]
	v_pk_mul_f32 v[168:169], v[130:131], s[8:9] op_sel_hi:[1,0]
	v_pk_mul_f32 v[14:15], v[136:137], s[8:9] op_sel_hi:[1,0]
	v_pk_mul_f32 v[12:13], v[134:135], s[8:9] op_sel_hi:[1,0]
	v_add_u32_e32 v3, 0x80, v10
	v_cvt_pk_bf16_f32 v12, v12, v13
	v_cvt_pk_bf16_f32 v13, v14, v15
	v_cvt_pk_bf16_f32 v14, v168, v169
	v_cvt_pk_bf16_f32 v15, v166, v167
	global_store_dwordx4 v[16:17], v[12:15], off offset:256
	v_pk_mul_f32 v[166:167], v[124:125], s[8:9] op_sel_hi:[1,0]
	v_pk_mul_f32 v[168:169], v[122:123], s[8:9] op_sel_hi:[1,0]
	v_mad_i64_i32 v[12:13], s[24:25], v8, s50, v[6:7]
	v_lshl_add_u64 v[12:13], v[12:13], 0, s[22:23]
	v_lshl_add_u64 v[16:17], v[12:13], 0, v[154:155]
	v_pk_mul_f32 v[14:15], v[128:129], s[8:9] op_sel_hi:[1,0]
	v_pk_mul_f32 v[12:13], v[126:127], s[8:9] op_sel_hi:[1,0]
	s_nop 0
	v_cvt_pk_bf16_f32 v12, v12, v13
	v_cvt_pk_bf16_f32 v13, v14, v15
	v_cvt_pk_bf16_f32 v14, v168, v169
	v_cvt_pk_bf16_f32 v15, v166, v167
	global_store_dwordx4 v[16:17], v[12:15], off
	v_pk_mul_f32 v[166:167], v[116:117], s[8:9] op_sel_hi:[1,0]
	v_pk_mul_f32 v[168:169], v[114:115], s[8:9] op_sel_hi:[1,0]
	v_pk_mul_f32 v[14:15], v[120:121], s[8:9] op_sel_hi:[1,0]
	v_pk_mul_f32 v[12:13], v[118:119], s[8:9] op_sel_hi:[1,0]
	s_nop 0
	v_cvt_pk_bf16_f32 v12, v12, v13
	v_cvt_pk_bf16_f32 v13, v14, v15
	v_cvt_pk_bf16_f32 v14, v168, v169
	v_cvt_pk_bf16_f32 v15, v166, v167
	global_store_dwordx4 v[16:17], v[12:15], off offset:256
	v_pk_mul_f32 v[166:167], v[108:109], s[8:9] op_sel_hi:[1,0]
	v_pk_mul_f32 v[168:169], v[106:107], s[8:9] op_sel_hi:[1,0]
	v_mad_i64_i32 v[12:13], s[24:25], v4, s50, v[6:7]
	v_lshl_add_u64 v[12:13], v[12:13], 0, s[22:23]
	v_lshl_add_u64 v[16:17], v[12:13], 0, v[154:155]
	v_pk_mul_f32 v[14:15], v[112:113], s[8:9] op_sel_hi:[1,0]
	v_pk_mul_f32 v[12:13], v[110:111], s[8:9] op_sel_hi:[1,0]
	s_nop 0
	v_cvt_pk_bf16_f32 v12, v12, v13
	v_cvt_pk_bf16_f32 v13, v14, v15
	v_cvt_pk_bf16_f32 v14, v168, v169
	v_cvt_pk_bf16_f32 v15, v166, v167
	global_store_dwordx4 v[16:17], v[12:15], off
	v_pk_mul_f32 v[166:167], v[100:101], s[8:9] op_sel_hi:[1,0]
	v_pk_mul_f32 v[168:169], v[98:99], s[8:9] op_sel_hi:[1,0]
	v_pk_mul_f32 v[14:15], v[104:105], s[8:9] op_sel_hi:[1,0]
	v_pk_mul_f32 v[12:13], v[102:103], s[8:9] op_sel_hi:[1,0]
	s_nop 0
	v_cvt_pk_bf16_f32 v12, v12, v13
	v_cvt_pk_bf16_f32 v13, v14, v15
	v_cvt_pk_bf16_f32 v14, v168, v169
	v_cvt_pk_bf16_f32 v15, v166, v167
	global_store_dwordx4 v[16:17], v[12:15], off offset:256
	v_pk_mul_f32 v[166:167], v[92:93], s[8:9] op_sel_hi:[1,0]
	v_pk_mul_f32 v[168:169], v[90:91], s[8:9] op_sel_hi:[1,0]
	v_mad_i64_i32 v[12:13], s[24:25], v2, s50, v[6:7]
	v_lshl_add_u64 v[12:13], v[12:13], 0, s[22:23]
	v_lshl_add_u64 v[16:17], v[12:13], 0, v[154:155]
	v_pk_mul_f32 v[14:15], v[96:97], s[8:9] op_sel_hi:[1,0]
	v_pk_mul_f32 v[12:13], v[94:95], s[8:9] op_sel_hi:[1,0]
	s_nop 0
	v_cvt_pk_bf16_f32 v12, v12, v13
	v_cvt_pk_bf16_f32 v13, v14, v15
	v_cvt_pk_bf16_f32 v14, v168, v169
	v_cvt_pk_bf16_f32 v15, v166, v167
	global_store_dwordx4 v[16:17], v[12:15], off
	v_pk_mul_f32 v[166:167], v[84:85], s[8:9] op_sel_hi:[1,0]
	v_pk_mul_f32 v[168:169], v[82:83], s[8:9] op_sel_hi:[1,0]
	v_pk_mul_f32 v[14:15], v[88:89], s[8:9] op_sel_hi:[1,0]
	v_pk_mul_f32 v[12:13], v[86:87], s[8:9] op_sel_hi:[1,0]
	s_nop 0
	v_cvt_pk_bf16_f32 v12, v12, v13
	v_cvt_pk_bf16_f32 v13, v14, v15
	v_cvt_pk_bf16_f32 v14, v168, v169
	v_cvt_pk_bf16_f32 v15, v166, v167
	global_store_dwordx4 v[16:17], v[12:15], off offset:256
	v_pk_mul_f32 v[166:167], v[76:77], s[8:9] op_sel_hi:[1,0]
	v_pk_mul_f32 v[168:169], v[74:75], s[8:9] op_sel_hi:[1,0]
	v_mad_i64_i32 v[12:13], s[24:25], v3, s50, v[6:7]
	v_lshl_add_u64 v[12:13], v[12:13], 0, s[22:23]
	v_lshl_add_u64 v[16:17], v[12:13], 0, v[154:155]
	v_pk_mul_f32 v[14:15], v[80:81], s[8:9] op_sel_hi:[1,0]
	v_pk_mul_f32 v[12:13], v[78:79], s[8:9] op_sel_hi:[1,0]
	v_add_u32_e32 v3, 0x90, v10
	v_cvt_pk_bf16_f32 v12, v12, v13
	v_cvt_pk_bf16_f32 v13, v14, v15
	v_cvt_pk_bf16_f32 v14, v168, v169
	v_cvt_pk_bf16_f32 v15, v166, v167
	global_store_dwordx4 v[16:17], v[12:15], off
	v_pk_mul_f32 v[166:167], v[68:69], s[8:9] op_sel_hi:[1,0]
	v_pk_mul_f32 v[168:169], v[66:67], s[8:9] op_sel_hi:[1,0]
	v_pk_mul_f32 v[14:15], v[72:73], s[8:9] op_sel_hi:[1,0]
	v_pk_mul_f32 v[12:13], v[70:71], s[8:9] op_sel_hi:[1,0]
	s_nop 0
	v_cvt_pk_bf16_f32 v12, v12, v13
	v_cvt_pk_bf16_f32 v13, v14, v15
	v_cvt_pk_bf16_f32 v14, v168, v169
	v_cvt_pk_bf16_f32 v15, v166, v167
	global_store_dwordx4 v[16:17], v[12:15], off offset:256
	v_pk_mul_f32 v[166:167], v[60:61], s[8:9] op_sel_hi:[1,0]
	v_pk_mul_f32 v[168:169], v[58:59], s[8:9] op_sel_hi:[1,0]
	v_mad_i64_i32 v[12:13], s[24:25], v3, s50, v[6:7]
	v_lshl_add_u64 v[12:13], v[12:13], 0, s[22:23]
	v_lshl_add_u64 v[16:17], v[12:13], 0, v[154:155]
	v_pk_mul_f32 v[14:15], v[64:65], s[8:9] op_sel_hi:[1,0]
	v_pk_mul_f32 v[12:13], v[62:63], s[8:9] op_sel_hi:[1,0]
	v_add_u32_e32 v3, 0xa0, v10
	v_cvt_pk_bf16_f32 v12, v12, v13
	v_cvt_pk_bf16_f32 v13, v14, v15
	v_cvt_pk_bf16_f32 v14, v168, v169
	v_cvt_pk_bf16_f32 v15, v166, v167
	global_store_dwordx4 v[16:17], v[12:15], off
	v_pk_mul_f32 v[166:167], v[48:49], s[8:9] op_sel_hi:[1,0]
	v_pk_mul_f32 v[168:169], v[46:47], s[8:9] op_sel_hi:[1,0]
	v_pk_mul_f32 v[14:15], v[56:57], s[8:9] op_sel_hi:[1,0]
	v_pk_mul_f32 v[12:13], v[54:55], s[8:9] op_sel_hi:[1,0]
	s_nop 0
	v_cvt_pk_bf16_f32 v12, v12, v13
	v_cvt_pk_bf16_f32 v13, v14, v15
	v_cvt_pk_bf16_f32 v14, v168, v169
	v_cvt_pk_bf16_f32 v15, v166, v167
	global_store_dwordx4 v[16:17], v[12:15], off offset:256
	v_pk_mul_f32 v[166:167], v[44:45], s[8:9] op_sel_hi:[1,0]
	v_pk_mul_f32 v[168:169], v[42:43], s[8:9] op_sel_hi:[1,0]
	v_mad_i64_i32 v[12:13], s[24:25], v3, s50, v[6:7]
	v_lshl_add_u64 v[12:13], v[12:13], 0, s[22:23]
	v_lshl_add_u64 v[16:17], v[12:13], 0, v[154:155]
	v_pk_mul_f32 v[14:15], v[52:53], s[8:9] op_sel_hi:[1,0]
	v_pk_mul_f32 v[12:13], v[50:51], s[8:9] op_sel_hi:[1,0]
	v_add_u32_e32 v3, 0xb0, v10
	v_cvt_pk_bf16_f32 v12, v12, v13
	v_cvt_pk_bf16_f32 v13, v14, v15
	v_cvt_pk_bf16_f32 v14, v168, v169
	v_cvt_pk_bf16_f32 v15, v166, v167
	global_store_dwordx4 v[16:17], v[12:15], off
	v_pk_mul_f32 v[166:167], v[32:33], s[8:9] op_sel_hi:[1,0]
	v_pk_mul_f32 v[168:169], v[30:31], s[8:9] op_sel_hi:[1,0]
	v_pk_mul_f32 v[14:15], v[40:41], s[8:9] op_sel_hi:[1,0]
	v_pk_mul_f32 v[12:13], v[38:39], s[8:9] op_sel_hi:[1,0]
	v_mad_i64_i32 v[6:7], s[24:25], v3, s50, v[6:7]
	v_cvt_pk_bf16_f32 v12, v12, v13
	v_cvt_pk_bf16_f32 v13, v14, v15
	v_cvt_pk_bf16_f32 v14, v168, v169
	v_cvt_pk_bf16_f32 v15, v166, v167
	global_store_dwordx4 v[16:17], v[12:15], off offset:256
	v_lshl_add_u64 v[6:7], v[6:7], 0, s[22:23]
	v_pk_mul_f32 v[16:17], v[28:29], s[8:9] op_sel_hi:[1,0]
	v_pk_mul_f32 v[14:15], v[36:37], s[8:9] op_sel_hi:[1,0]
	v_pk_mul_f32 v[12:13], v[34:35], s[8:9] op_sel_hi:[1,0]
	v_pk_mul_f32 v[166:167], v[26:27], s[8:9] op_sel_hi:[1,0]
	v_lshl_add_u64 v[6:7], v[6:7], 0, v[154:155]
	v_cvt_pk_bf16_f32 v12, v12, v13
	v_cvt_pk_bf16_f32 v13, v14, v15
	v_cvt_pk_bf16_f32 v14, v166, v167
	v_cvt_pk_bf16_f32 v15, v16, v17
	global_store_dwordx4 v[6:7], v[12:15], off
	v_pk_mul_f32 v[16:17], v[20:21], s[8:9] op_sel_hi:[1,0]
	v_pk_mul_f32 v[166:167], v[18:19], s[8:9] op_sel_hi:[1,0]
	v_pk_mul_f32 v[14:15], v[24:25], s[8:9] op_sel_hi:[1,0]
	v_pk_mul_f32 v[12:13], v[22:23], s[8:9] op_sel_hi:[1,0]
	s_mov_b64 s[22:23], 0
	v_cvt_pk_bf16_f32 v12, v12, v13
	v_cvt_pk_bf16_f32 v13, v14, v15
	v_cvt_pk_bf16_f32 v14, v166, v167
	v_cvt_pk_bf16_f32 v15, v16, v17
	global_store_dwordx4 v[6:7], v[12:15], off offset:256

.LBB0_1230:
	ds_read_b128 v[2:5], v190
	ds_read_b128 v[6:9], v190 offset:1024
	ds_read_b128 v[10:13], v190 offset:2048
	ds_read_b128 v[14:17], v190 offset:3072
	s_add_u32 s26, s24, 0xfffc0080
	s_addc_u32 s27, s25, -1
	s_cmp_eq_u32 s48, 12
	s_cselect_b32 s29, s6, s27
	s_cselect_b32 s28, s17, s26
	s_cselect_b32 s27, s15, s31
	s_cselect_b32 s26, s23, s30
	s_add_i32 m0, s35, 0xc000
	ds_read_b128 v[194:197], v191
	ds_read_b128 v[198:201], v191 offset:1024
	ds_read_b128 v[214:217], v191 offset:2048
	ds_read_b128 v[218:221], v191 offset:3072
	ds_read_b128 v[222:225], v191 offset:4096
	ds_read_b128 v[226:229], v191 offset:5120
	ds_read_b128 v[230:233], v191 offset:6144
	ds_read_b128 v[234:237], v191 offset:7168
	global_load_lds_dwordx4 v170, s[24:25]
	s_add_i32 m0, s35, 0xe000
	s_nop 0
	global_load_lds_dwordx4 v172, s[24:25]
	s_waitcnt lgkmcnt(8)
	s_barrier
	s_waitcnt lgkmcnt(0)
	s_setprio 1
	s_waitcnt lgkmcnt(0)
	v_mfma_scale_f32_16x16x128_f8f6f4 v[142:145], v[2:9], v[194:201], v[142:145], v192, v192 op_sel_hi:[0,0,0]
	v_mfma_scale_f32_16x16x128_f8f6f4 v[138:141], v[10:17], v[194:201], v[138:141], v192, v192 op_sel_hi:[0,0,0]
	v_mfma_scale_f32_16x16x128_f8f6f4 v[126:129], v[2:9], v[214:221], v[126:129], v192, v192 op_sel_hi:[0,0,0]
	v_mfma_scale_f32_16x16x128_f8f6f4 v[122:125], v[10:17], v[214:221], v[122:125], v192, v192 op_sel_hi:[0,0,0]
	v_mfma_scale_f32_16x16x128_f8f6f4 v[110:113], v[2:9], v[222:229], v[110:113], v192, v192 op_sel_hi:[0,0,0]
	v_mfma_scale_f32_16x16x128_f8f6f4 v[106:109], v[10:17], v[222:229], v[106:109], v192, v192 op_sel_hi:[0,0,0]
	v_mfma_scale_f32_16x16x128_f8f6f4 v[94:97], v[2:9], v[230:237], v[94:97], v192, v192 op_sel_hi:[0,0,0]
	v_mfma_scale_f32_16x16x128_f8f6f4 v[90:93], v[10:17], v[230:237], v[90:93], v192, v192 op_sel_hi:[0,0,0]
	s_setprio 0
	s_barrier
	s_add_i32 s49, s44, s34
	s_add_u32 s66, s26, 0x80
	s_addc_u32 s67, s27, 0
	s_mov_b32 m0, s49
	ds_read_b128 v[238:241], v193
	ds_read_b128 v[242:245], v193 offset:1024
	ds_read_b128 v[246:249], v193 offset:2048
	ds_read_b128 v[250:253], v193 offset:3072
	global_load_lds_dwordx4 v148, s[26:27]
	s_add_i32 m0, s49, 0x2000
	s_nop 0
	global_load_lds_dwordx4 v152, s[26:27]
	s_barrier
	s_waitcnt lgkmcnt(0)
	s_setprio 1
	s_waitcnt lgkmcnt(0)
	v_mfma_scale_f32_16x16x128_f8f6f4 v[134:137], v[238:245], v[194:201], v[134:137], v192, v192 op_sel_hi:[0,0,0]
	v_mfma_scale_f32_16x16x128_f8f6f4 v[130:133], v[246:253], v[194:201], v[130:133], v192, v192 op_sel_hi:[0,0,0]
	v_mfma_scale_f32_16x16x128_f8f6f4 v[118:121], v[238:245], v[214:221], v[118:121], v192, v192 op_sel_hi:[0,0,0]
	v_mfma_scale_f32_16x16x128_f8f6f4 v[114:117], v[246:253], v[214:221], v[114:117], v192, v192 op_sel_hi:[0,0,0]
	v_mfma_scale_f32_16x16x128_f8f6f4 v[102:105], v[238:245], v[222:229], v[102:105], v192, v192 op_sel_hi:[0,0,0]
	v_mfma_scale_f32_16x16x128_f8f6f4 v[98:101], v[246:253], v[222:229], v[98:101], v192, v192 op_sel_hi:[0,0,0]
	v_mfma_scale_f32_16x16x128_f8f6f4 v[86:89], v[238:245], v[230:237], v[86:89], v192, v192 op_sel_hi:[0,0,0]
	v_mfma_scale_f32_16x16x128_f8f6f4 v[82:85], v[246:253], v[230:237], v[82:85], v192, v192 op_sel_hi:[0,0,0]
	s_setprio 0
	s_mov_b32 m0, s35
	s_add_u32 s68, s28, 0x80
	s_addc_u32 s69, s29, 0
	s_barrier
	ds_read_b128 v[194:197], v191 offset:16384
	ds_read_b128 v[198:201], v191 offset:17408
	ds_read_b128 v[214:217], v191 offset:18432
	ds_read_b128 v[218:221], v191 offset:19456
	ds_read_b128 v[222:225], v191 offset:20480
	ds_read_b128 v[226:229], v191 offset:21504
	ds_read_b128 v[230:233], v191 offset:22528
	ds_read_b128 v[234:237], v191 offset:23552
	global_load_lds_dwordx4 v146, s[28:29]
	s_mov_b32 m0, s36
	s_nop 0
	global_load_lds_dwordx4 v150, s[28:29]
	s_barrier
	s_waitcnt lgkmcnt(0)
	s_setprio 1
	s_waitcnt lgkmcnt(0)
	v_mfma_scale_f32_16x16x128_f8f6f4 v[78:81], v[2:9], v[194:201], v[78:81], v192, v192 op_sel_hi:[0,0,0]
	v_mfma_scale_f32_16x16x128_f8f6f4 v[74:77], v[10:17], v[194:201], v[74:77], v192, v192 op_sel_hi:[0,0,0]
	v_mfma_scale_f32_16x16x128_f8f6f4 v[62:65], v[2:9], v[214:221], v[62:65], v192, v192 op_sel_hi:[0,0,0]
	v_mfma_scale_f32_16x16x128_f8f6f4 v[58:61], v[10:17], v[214:221], v[58:61], v192, v192 op_sel_hi:[0,0,0]
	v_mfma_scale_f32_16x16x128_f8f6f4 v[46:49], v[2:9], v[222:229], v[46:49], v192, v192 op_sel_hi:[0,0,0]
	v_mfma_scale_f32_16x16x128_f8f6f4 v[42:45], v[10:17], v[222:229], v[42:45], v192, v192 op_sel_hi:[0,0,0]
	v_mfma_scale_f32_16x16x128_f8f6f4 v[30:33], v[2:9], v[230:237], v[30:33], v192, v192 op_sel_hi:[0,0,0]
	v_mfma_scale_f32_16x16x128_f8f6f4 v[26:29], v[10:17], v[230:237], v[26:29], v192, v192 op_sel_hi:[0,0,0]
	s_setprio 0
	s_barrier
	s_add_u32 s50, s26, 0x40000
	s_addc_u32 s51, s27, 0
	s_add_i32 s49, s45, s34
	s_mov_b32 m0, s49
	s_nop 0
	global_load_lds_dwordx4 v148, s[50:51]
	s_add_i32 m0, s49, 0x2000
	s_nop 0
	global_load_lds_dwordx4 v152, s[50:51]
	s_waitcnt vmcnt(6)
	s_barrier
	s_setprio 1
	v_mfma_scale_f32_16x16x128_f8f6f4 v[70:73], v[238:245], v[194:201], v[70:73], v192, v192 op_sel_hi:[0,0,0]
	v_mfma_scale_f32_16x16x128_f8f6f4 v[66:69], v[246:253], v[194:201], v[66:69], v192, v192 op_sel_hi:[0,0,0]
	v_mfma_scale_f32_16x16x128_f8f6f4 v[54:57], v[238:245], v[214:221], v[54:57], v192, v192 op_sel_hi:[0,0,0]
	v_mfma_scale_f32_16x16x128_f8f6f4 v[50:53], v[246:253], v[214:221], v[50:53], v192, v192 op_sel_hi:[0,0,0]
	v_mfma_scale_f32_16x16x128_f8f6f4 v[38:41], v[238:245], v[222:229], v[38:41], v192, v192 op_sel_hi:[0,0,0]
	v_mfma_scale_f32_16x16x128_f8f6f4 v[34:37], v[246:253], v[222:229], v[34:37], v192, v192 op_sel_hi:[0,0,0]
	v_mfma_scale_f32_16x16x128_f8f6f4 v[22:25], v[238:245], v[230:237], v[22:25], v192, v192 op_sel_hi:[0,0,0]
	v_mfma_scale_f32_16x16x128_f8f6f4 v[18:21], v[246:253], v[230:237], v[18:21], v192, v192 op_sel_hi:[0,0,0]
	s_setprio 0
	s_add_i32 s49, 0, 0x18000
	v_add_u32_e32 v14, s49, v186
	s_barrier
	ds_read_b128 v[2:5], v14
	ds_read_b128 v[6:9], v14 offset:1024
	ds_read_b128 v[10:13], v14 offset:2048
	ds_read_b128 v[14:17], v14 offset:3072
	s_add_u32 s28, s28, 0x40000
	s_addc_u32 s29, s29, 0
	s_mov_b32 m0, s37
	ds_read_b128 v[194:197], v191 offset:32768
	ds_read_b128 v[198:201], v191 offset:33792
	ds_read_b128 v[214:217], v191 offset:34816
	ds_read_b128 v[218:221], v191 offset:35840
	ds_read_b128 v[222:225], v191 offset:36864
	ds_read_b128 v[226:229], v191 offset:37888
	ds_read_b128 v[230:233], v191 offset:38912
	ds_read_b128 v[234:237], v191 offset:39936
	global_load_lds_dwordx4 v146, s[28:29]
	s_mov_b32 m0, s38
	s_nop 0
	global_load_lds_dwordx4 v150, s[28:29]
	s_waitcnt lgkmcnt(8)
	s_barrier
	s_waitcnt lgkmcnt(0)
	s_setprio 1
	s_waitcnt lgkmcnt(0)
	v_mfma_scale_f32_16x16x128_f8f6f4 v[142:145], v[2:9], v[194:201], v[142:145], v192, v192 op_sel_hi:[0,0,0]
	v_mfma_scale_f32_16x16x128_f8f6f4 v[138:141], v[10:17], v[194:201], v[138:141], v192, v192 op_sel_hi:[0,0,0]
	v_mfma_scale_f32_16x16x128_f8f6f4 v[126:129], v[2:9], v[214:221], v[126:129], v192, v192 op_sel_hi:[0,0,0]
	v_mfma_scale_f32_16x16x128_f8f6f4 v[122:125], v[10:17], v[214:221], v[122:125], v192, v192 op_sel_hi:[0,0,0]
	v_mfma_scale_f32_16x16x128_f8f6f4 v[110:113], v[2:9], v[222:229], v[110:113], v192, v192 op_sel_hi:[0,0,0]
	v_mfma_scale_f32_16x16x128_f8f6f4 v[106:109], v[10:17], v[222:229], v[106:109], v192, v192 op_sel_hi:[0,0,0]
	v_mfma_scale_f32_16x16x128_f8f6f4 v[94:97], v[2:9], v[230:237], v[94:97], v192, v192 op_sel_hi:[0,0,0]
	v_mfma_scale_f32_16x16x128_f8f6f4 v[90:93], v[10:17], v[230:237], v[90:93], v192, v192 op_sel_hi:[0,0,0]
	s_setprio 0
	s_barrier
	s_add_i32 s28, 0, 0x1c000
	s_add_i32 s29, s49, s34
	v_add_u32_e32 v202, s28, v186
	s_mov_b32 m0, s29
	ds_read_b128 v[238:241], v202
	ds_read_b128 v[242:245], v202 offset:1024
	ds_read_b128 v[246:249], v202 offset:2048
	ds_read_b128 v[250:253], v202 offset:3072
	global_load_lds_dwordx4 v148, s[66:67]
	s_add_i32 m0, s29, 0x2000
	s_nop 0
	global_load_lds_dwordx4 v152, s[66:67]
	s_barrier
	s_waitcnt lgkmcnt(0)
	s_setprio 1
	s_waitcnt lgkmcnt(0)
	v_mfma_scale_f32_16x16x128_f8f6f4 v[134:137], v[238:245], v[194:201], v[134:137], v192, v192 op_sel_hi:[0,0,0]
	v_mfma_scale_f32_16x16x128_f8f6f4 v[130:133], v[246:253], v[194:201], v[130:133], v192, v192 op_sel_hi:[0,0,0]
	v_mfma_scale_f32_16x16x128_f8f6f4 v[118:121], v[238:245], v[214:221], v[118:121], v192, v192 op_sel_hi:[0,0,0]
	v_mfma_scale_f32_16x16x128_f8f6f4 v[114:117], v[246:253], v[214:221], v[114:117], v192, v192 op_sel_hi:[0,0,0]
	v_mfma_scale_f32_16x16x128_f8f6f4 v[102:105], v[238:245], v[222:229], v[102:105], v192, v192 op_sel_hi:[0,0,0]
	v_mfma_scale_f32_16x16x128_f8f6f4 v[98:101], v[246:253], v[222:229], v[98:101], v192, v192 op_sel_hi:[0,0,0]
	v_mfma_scale_f32_16x16x128_f8f6f4 v[86:89], v[238:245], v[230:237], v[86:89], v192, v192 op_sel_hi:[0,0,0]
	v_mfma_scale_f32_16x16x128_f8f6f4 v[82:85], v[246:253], v[230:237], v[82:85], v192, v192 op_sel_hi:[0,0,0]
	s_setprio 0
	s_mov_b32 m0, s41
	s_barrier
	ds_read_b128 v[194:197], v191 offset:49152
	ds_read_b128 v[198:201], v191 offset:50176
	ds_read_b128 v[214:217], v191 offset:51200
	ds_read_b128 v[218:221], v191 offset:52224
	ds_read_b128 v[222:225], v191 offset:53248
	ds_read_b128 v[226:229], v191 offset:54272
	ds_read_b128 v[230:233], v191 offset:55296
	ds_read_b128 v[234:237], v191 offset:56320
	global_load_lds_dwordx4 v146, s[68:69]
	s_mov_b32 m0, s42
	s_nop 0
	global_load_lds_dwordx4 v150, s[68:69]
	s_barrier
	s_waitcnt lgkmcnt(0)
	s_setprio 1
	s_waitcnt lgkmcnt(0)
	v_mfma_scale_f32_16x16x128_f8f6f4 v[78:81], v[2:9], v[194:201], v[78:81], v192, v192 op_sel_hi:[0,0,0]
	v_mfma_scale_f32_16x16x128_f8f6f4 v[74:77], v[10:17], v[194:201], v[74:77], v192, v192 op_sel_hi:[0,0,0]
	v_mfma_scale_f32_16x16x128_f8f6f4 v[62:65], v[2:9], v[214:221], v[62:65], v192, v192 op_sel_hi:[0,0,0]
	v_mfma_scale_f32_16x16x128_f8f6f4 v[58:61], v[10:17], v[214:221], v[58:61], v192, v192 op_sel_hi:[0,0,0]
	v_mfma_scale_f32_16x16x128_f8f6f4 v[46:49], v[2:9], v[222:229], v[46:49], v192, v192 op_sel_hi:[0,0,0]
	v_mfma_scale_f32_16x16x128_f8f6f4 v[42:45], v[10:17], v[222:229], v[42:45], v192, v192 op_sel_hi:[0,0,0]
	v_mfma_scale_f32_16x16x128_f8f6f4 v[30:33], v[2:9], v[230:237], v[30:33], v192, v192 op_sel_hi:[0,0,0]
	v_mfma_scale_f32_16x16x128_f8f6f4 v[26:29], v[10:17], v[230:237], v[26:29], v192, v192 op_sel_hi:[0,0,0]
	s_setprio 0
	s_barrier
	s_add_u32 s26, s26, 0x40080
	s_addc_u32 s27, s27, 0
	s_add_i32 s28, s28, s34
	s_mov_b32 m0, s28
	s_nop 0
	global_load_lds_dwordx4 v148, s[26:27]
	s_add_i32 m0, s28, 0x2000
	s_nop 0
	global_load_lds_dwordx4 v152, s[26:27]
	s_waitcnt vmcnt(6)
	s_barrier
	s_setprio 1
	v_mfma_scale_f32_16x16x128_f8f6f4 v[70:73], v[238:245], v[194:201], v[70:73], v192, v192 op_sel_hi:[0,0,0]
	v_mfma_scale_f32_16x16x128_f8f6f4 v[66:69], v[246:253], v[194:201], v[66:69], v192, v192 op_sel_hi:[0,0,0]
	v_mfma_scale_f32_16x16x128_f8f6f4 v[54:57], v[238:245], v[214:221], v[54:57], v192, v192 op_sel_hi:[0,0,0]
	v_mfma_scale_f32_16x16x128_f8f6f4 v[50:53], v[246:253], v[214:221], v[50:53], v192, v192 op_sel_hi:[0,0,0]
	v_mfma_scale_f32_16x16x128_f8f6f4 v[38:41], v[238:245], v[222:229], v[38:41], v192, v192 op_sel_hi:[0,0,0]
	v_mfma_scale_f32_16x16x128_f8f6f4 v[34:37], v[246:253], v[222:229], v[34:37], v192, v192 op_sel_hi:[0,0,0]
	v_mfma_scale_f32_16x16x128_f8f6f4 v[22:25], v[238:245], v[230:237], v[22:25], v192, v192 op_sel_hi:[0,0,0]
	v_mfma_scale_f32_16x16x128_f8f6f4 v[18:21], v[246:253], v[230:237], v[18:21], v192, v192 op_sel_hi:[0,0,0]
	s_setprio 0
	s_add_i32 s48, s48, 2
	s_add_u32 s24, s24, 0x100
	s_addc_u32 s25, s25, 0
	s_add_u32 s30, s30, 0x100
	s_addc_u32 s31, s31, 0
	s_cmp_gt_u32 s48, 13
	s_barrier
	s_cbranch_scc0 .LBB0_1230
	s_lshl_b32 s26, s22, 8
	s_cmpk_gt_i32 s22, 0x7f
	s_mov_b64 s[30:31], -1
	s_cbranch_scc0 .LBB0_1233
	s_add_i32 s6, s26, 0xffff8000
	s_mov_b32 s27, s7
	s_lshl_b64 s[28:29], s[6:7], 12
	s_lshl_b64 s[24:25], s[26:27], 12
	s_mov_b64 s[30:31], 0

.LBB0_1369:
	ds_read_b128 v[152:155], v149
	ds_read_b128 v[156:159], v149 offset:1024
	ds_read_b128 v[160:163], v149 offset:2048
	ds_read_b128 v[164:167], v149 offset:3072
	s_add_u32 s28, s26, 0xfff80080
	s_addc_u32 s29, s27, -1
	s_cmp_eq_u32 s54, 28
	s_cselect_b32 s31, s21, s29
	s_cselect_b32 s30, s50, s28
	s_cselect_b32 s29, s19, s53
	s_cselect_b32 s28, s51, s52
	s_add_i32 m0, s17, 0xc000
	ds_read_b128 v[168:171], v150
	ds_read_b128 v[172:175], v150 offset:1024
	ds_read_b128 v[176:179], v150 offset:2048
	ds_read_b128 v[180:183], v150 offset:3072
	ds_read_b128 v[184:187], v150 offset:4096
	ds_read_b128 v[190:193], v150 offset:5120
	ds_read_b128 v[194:197], v150 offset:6144
	ds_read_b128 v[198:201], v150 offset:7168
	global_load_lds_dwordx4 v138, s[26:27]
	s_add_i32 m0, s17, 0xe000
	s_nop 0
	global_load_lds_dwordx4 v140, s[26:27]
	s_waitcnt lgkmcnt(8)
	s_barrier
	s_waitcnt lgkmcnt(0)
	s_setprio 1
	s_waitcnt lgkmcnt(0)
	v_mfma_f32_16x16x32_bf16 v[126:129], v[152:155], v[168:171], v[126:129]
	v_mfma_f32_16x16x32_bf16 v[122:125], v[160:163], v[168:171], v[122:125]
	v_mfma_f32_16x16x32_bf16 v[118:121], v[152:155], v[176:179], v[118:121]
	v_mfma_f32_16x16x32_bf16 v[114:117], v[160:163], v[176:179], v[114:117]
	v_mfma_f32_16x16x32_bf16 v[102:105], v[152:155], v[184:187], v[102:105]
	v_mfma_f32_16x16x32_bf16 v[98:101], v[160:163], v[184:187], v[98:101]
	v_mfma_f32_16x16x32_bf16 v[86:89], v[152:155], v[194:197], v[86:89]
	v_mfma_f32_16x16x32_bf16 v[82:85], v[160:163], v[194:197], v[82:85]
	v_mfma_f32_16x16x32_bf16 v[126:129], v[156:159], v[172:175], v[126:129]
	v_mfma_f32_16x16x32_bf16 v[122:125], v[164:167], v[172:175], v[122:125]
	v_mfma_f32_16x16x32_bf16 v[118:121], v[156:159], v[180:183], v[118:121]
	v_mfma_f32_16x16x32_bf16 v[114:117], v[164:167], v[180:183], v[114:117]
	v_mfma_f32_16x16x32_bf16 v[102:105], v[156:159], v[190:193], v[102:105]
	v_mfma_f32_16x16x32_bf16 v[98:101], v[164:167], v[190:193], v[98:101]
	v_mfma_f32_16x16x32_bf16 v[86:89], v[156:159], v[198:201], v[86:89]
	v_mfma_f32_16x16x32_bf16 v[82:85], v[164:167], v[198:201], v[82:85]
	s_setprio 0
	s_barrier
	s_add_i32 s55, s43, s35
	s_add_u32 s66, s28, 0x80
	s_addc_u32 s67, s29, 0
	s_mov_b32 m0, s55
	ds_read_b128 v[214:217], v151
	ds_read_b128 v[218:221], v151 offset:1024
	ds_read_b128 v[222:225], v151 offset:2048
	ds_read_b128 v[226:229], v151 offset:3072
	global_load_lds_dwordx4 v132, s[28:29]
	s_add_i32 m0, s55, 0x2000
	s_nop 0
	global_load_lds_dwordx4 v136, s[28:29]
	s_barrier
	s_waitcnt lgkmcnt(0)
	s_setprio 1
	s_waitcnt lgkmcnt(0)
	v_mfma_f32_16x16x32_bf16 v[110:113], v[214:217], v[168:171], v[110:113]
	v_mfma_f32_16x16x32_bf16 v[106:109], v[222:225], v[168:171], v[106:109]
	v_mfma_f32_16x16x32_bf16 v[94:97], v[214:217], v[176:179], v[94:97]
	v_mfma_f32_16x16x32_bf16 v[90:93], v[222:225], v[176:179], v[90:93]
	v_mfma_f32_16x16x32_bf16 v[78:81], v[214:217], v[184:187], v[78:81]
	v_mfma_f32_16x16x32_bf16 v[74:77], v[222:225], v[184:187], v[74:77]
	v_mfma_f32_16x16x32_bf16 v[70:73], v[214:217], v[194:197], v[70:73]
	v_mfma_f32_16x16x32_bf16 v[66:69], v[222:225], v[194:197], v[66:69]
	v_mfma_f32_16x16x32_bf16 v[110:113], v[218:221], v[172:175], v[110:113]
	v_mfma_f32_16x16x32_bf16 v[106:109], v[226:229], v[172:175], v[106:109]
	v_mfma_f32_16x16x32_bf16 v[94:97], v[218:221], v[180:183], v[94:97]
	v_mfma_f32_16x16x32_bf16 v[90:93], v[226:229], v[180:183], v[90:93]
	v_mfma_f32_16x16x32_bf16 v[78:81], v[218:221], v[190:193], v[78:81]
	v_mfma_f32_16x16x32_bf16 v[74:77], v[226:229], v[190:193], v[74:77]
	v_mfma_f32_16x16x32_bf16 v[70:73], v[218:221], v[198:201], v[70:73]
	v_mfma_f32_16x16x32_bf16 v[66:69], v[226:229], v[198:201], v[66:69]
	s_setprio 0
	s_mov_b32 m0, s17
	s_add_u32 s68, s30, 0x80
	s_addc_u32 s69, s31, 0
	s_barrier
	ds_read_b128 v[168:171], v150 offset:16384
	ds_read_b128 v[172:175], v150 offset:17408
	ds_read_b128 v[176:179], v150 offset:18432
	ds_read_b128 v[180:183], v150 offset:19456
	ds_read_b128 v[184:187], v150 offset:20480
	ds_read_b128 v[190:193], v150 offset:21504
	ds_read_b128 v[194:197], v150 offset:22528
	ds_read_b128 v[198:201], v150 offset:23552
	global_load_lds_dwordx4 v130, s[30:31]
	s_mov_b32 m0, s36
	s_nop 0
	global_load_lds_dwordx4 v134, s[30:31]
	s_barrier
	s_waitcnt lgkmcnt(0)
	s_setprio 1
	s_waitcnt lgkmcnt(0)
	v_mfma_f32_16x16x32_bf16 v[62:65], v[152:155], v[168:171], v[62:65]
	v_mfma_f32_16x16x32_bf16 v[58:61], v[160:163], v[168:171], v[58:61]
	v_mfma_f32_16x16x32_bf16 v[54:57], v[152:155], v[176:179], v[54:57]
	v_mfma_f32_16x16x32_bf16 v[50:53], v[160:163], v[176:179], v[50:53]
	v_mfma_f32_16x16x32_bf16 v[38:41], v[152:155], v[184:187], v[38:41]
	v_mfma_f32_16x16x32_bf16 v[34:37], v[160:163], v[184:187], v[34:37]
	v_mfma_f32_16x16x32_bf16 v[22:25], v[152:155], v[194:197], v[22:25]
	v_mfma_f32_16x16x32_bf16 v[18:21], v[160:163], v[194:197], v[18:21]
	v_mfma_f32_16x16x32_bf16 v[62:65], v[156:159], v[172:175], v[62:65]
	v_mfma_f32_16x16x32_bf16 v[58:61], v[164:167], v[172:175], v[58:61]
	v_mfma_f32_16x16x32_bf16 v[54:57], v[156:159], v[180:183], v[54:57]
	v_mfma_f32_16x16x32_bf16 v[50:53], v[164:167], v[180:183], v[50:53]
	v_mfma_f32_16x16x32_bf16 v[38:41], v[156:159], v[190:193], v[38:41]
	v_mfma_f32_16x16x32_bf16 v[34:37], v[164:167], v[190:193], v[34:37]
	v_mfma_f32_16x16x32_bf16 v[22:25], v[156:159], v[198:201], v[22:25]
	v_mfma_f32_16x16x32_bf16 v[18:21], v[164:167], v[198:201], v[18:21]
	s_setprio 0
	s_barrier
	s_add_u32 s56, s28, 0x80000
	s_addc_u32 s57, s29, 0
	s_add_i32 s55, s44, s35
	s_mov_b32 m0, s55
	s_nop 0
	global_load_lds_dwordx4 v132, s[56:57]
	s_add_i32 m0, s55, 0x2000
	s_nop 0
	global_load_lds_dwordx4 v136, s[56:57]
	s_waitcnt vmcnt(6)
	s_barrier
	s_setprio 1
	v_mfma_f32_16x16x32_bf16 v[46:49], v[214:217], v[168:171], v[46:49]
	v_mfma_f32_16x16x32_bf16 v[42:45], v[222:225], v[168:171], v[42:45]
	v_mfma_f32_16x16x32_bf16 v[30:33], v[214:217], v[176:179], v[30:33]
	v_mfma_f32_16x16x32_bf16 v[26:29], v[222:225], v[176:179], v[26:29]
	v_mfma_f32_16x16x32_bf16 v[14:17], v[214:217], v[184:187], v[14:17]
	v_mfma_f32_16x16x32_bf16 v[10:13], v[222:225], v[184:187], v[10:13]
	v_mfma_f32_16x16x32_bf16 v[6:9], v[214:217], v[194:197], v[6:9]
	v_mfma_f32_16x16x32_bf16 v[2:5], v[222:225], v[194:197], v[2:5]
	v_mfma_f32_16x16x32_bf16 v[46:49], v[218:221], v[172:175], v[46:49]
	v_mfma_f32_16x16x32_bf16 v[42:45], v[226:229], v[172:175], v[42:45]
	v_mfma_f32_16x16x32_bf16 v[30:33], v[218:221], v[180:183], v[30:33]
	v_mfma_f32_16x16x32_bf16 v[26:29], v[226:229], v[180:183], v[26:29]
	v_mfma_f32_16x16x32_bf16 v[14:17], v[218:221], v[190:193], v[14:17]
	v_mfma_f32_16x16x32_bf16 v[10:13], v[226:229], v[190:193], v[10:13]
	v_mfma_f32_16x16x32_bf16 v[6:9], v[218:221], v[198:201], v[6:9]
	v_mfma_f32_16x16x32_bf16 v[2:5], v[226:229], v[198:201], v[2:5]
	s_setprio 0
	s_add_i32 s55, 0, 0x18000
	v_add_u32_e32 v164, s55, v147
	s_barrier
	ds_read_b128 v[152:155], v164
	ds_read_b128 v[156:159], v164 offset:1024
	ds_read_b128 v[160:163], v164 offset:2048
	ds_read_b128 v[164:167], v164 offset:3072
	s_add_u32 s30, s30, 0x80000
	s_addc_u32 s31, s31, 0
	s_mov_b32 m0, s37
	ds_read_b128 v[168:171], v150 offset:32768
	ds_read_b128 v[172:175], v150 offset:33792
	ds_read_b128 v[176:179], v150 offset:34816
	ds_read_b128 v[180:183], v150 offset:35840
	ds_read_b128 v[184:187], v150 offset:36864
	ds_read_b128 v[190:193], v150 offset:37888
	ds_read_b128 v[194:197], v150 offset:38912
	ds_read_b128 v[198:201], v150 offset:39936
	global_load_lds_dwordx4 v130, s[30:31]
	s_mov_b32 m0, s38
	s_nop 0
	global_load_lds_dwordx4 v134, s[30:31]
	s_waitcnt lgkmcnt(8)
	s_barrier
	s_waitcnt lgkmcnt(0)
	s_setprio 1
	s_waitcnt lgkmcnt(0)
	v_mfma_f32_16x16x32_bf16 v[126:129], v[152:155], v[168:171], v[126:129]
	v_mfma_f32_16x16x32_bf16 v[122:125], v[160:163], v[168:171], v[122:125]
	v_mfma_f32_16x16x32_bf16 v[118:121], v[152:155], v[176:179], v[118:121]
	v_mfma_f32_16x16x32_bf16 v[114:117], v[160:163], v[176:179], v[114:117]
	v_mfma_f32_16x16x32_bf16 v[102:105], v[152:155], v[184:187], v[102:105]
	v_mfma_f32_16x16x32_bf16 v[98:101], v[160:163], v[184:187], v[98:101]
	v_mfma_f32_16x16x32_bf16 v[86:89], v[152:155], v[194:197], v[86:89]
	v_mfma_f32_16x16x32_bf16 v[82:85], v[160:163], v[194:197], v[82:85]
	v_mfma_f32_16x16x32_bf16 v[126:129], v[156:159], v[172:175], v[126:129]
	v_mfma_f32_16x16x32_bf16 v[122:125], v[164:167], v[172:175], v[122:125]
	v_mfma_f32_16x16x32_bf16 v[118:121], v[156:159], v[180:183], v[118:121]
	v_mfma_f32_16x16x32_bf16 v[114:117], v[164:167], v[180:183], v[114:117]
	v_mfma_f32_16x16x32_bf16 v[102:105], v[156:159], v[190:193], v[102:105]
	v_mfma_f32_16x16x32_bf16 v[98:101], v[164:167], v[190:193], v[98:101]
	v_mfma_f32_16x16x32_bf16 v[86:89], v[156:159], v[198:201], v[86:89]
	v_mfma_f32_16x16x32_bf16 v[82:85], v[164:167], v[198:201], v[82:85]
	s_setprio 0
	s_barrier
	s_add_i32 s30, 0, 0x1c000
	s_add_i32 s31, s55, s35
	v_add_u32_e32 v213, s30, v147
	s_mov_b32 m0, s31
	ds_read_b128 v[214:217], v213
	ds_read_b128 v[218:221], v213 offset:1024
	ds_read_b128 v[222:225], v213 offset:2048
	ds_read_b128 v[226:229], v213 offset:3072
	global_load_lds_dwordx4 v132, s[66:67]
	s_add_i32 m0, s31, 0x2000
	s_nop 0
	global_load_lds_dwordx4 v136, s[66:67]
	s_barrier
	s_waitcnt lgkmcnt(0)
	s_setprio 1
	s_waitcnt lgkmcnt(0)
	v_mfma_f32_16x16x32_bf16 v[110:113], v[214:217], v[168:171], v[110:113]
	v_mfma_f32_16x16x32_bf16 v[106:109], v[222:225], v[168:171], v[106:109]
	v_mfma_f32_16x16x32_bf16 v[94:97], v[214:217], v[176:179], v[94:97]
	v_mfma_f32_16x16x32_bf16 v[90:93], v[222:225], v[176:179], v[90:93]
	v_mfma_f32_16x16x32_bf16 v[78:81], v[214:217], v[184:187], v[78:81]
	v_mfma_f32_16x16x32_bf16 v[74:77], v[222:225], v[184:187], v[74:77]
	v_mfma_f32_16x16x32_bf16 v[70:73], v[214:217], v[194:197], v[70:73]
	v_mfma_f32_16x16x32_bf16 v[66:69], v[222:225], v[194:197], v[66:69]
	v_mfma_f32_16x16x32_bf16 v[110:113], v[218:221], v[172:175], v[110:113]
	v_mfma_f32_16x16x32_bf16 v[106:109], v[226:229], v[172:175], v[106:109]
	v_mfma_f32_16x16x32_bf16 v[94:97], v[218:221], v[180:183], v[94:97]
	v_mfma_f32_16x16x32_bf16 v[90:93], v[226:229], v[180:183], v[90:93]
	v_mfma_f32_16x16x32_bf16 v[78:81], v[218:221], v[190:193], v[78:81]
	v_mfma_f32_16x16x32_bf16 v[74:77], v[226:229], v[190:193], v[74:77]
	v_mfma_f32_16x16x32_bf16 v[70:73], v[218:221], v[198:201], v[70:73]
	v_mfma_f32_16x16x32_bf16 v[66:69], v[226:229], v[198:201], v[66:69]
	s_setprio 0
	s_mov_b32 m0, s40
	s_barrier
	ds_read_b128 v[168:171], v150 offset:49152
	ds_read_b128 v[172:175], v150 offset:50176
	ds_read_b128 v[176:179], v150 offset:51200
	ds_read_b128 v[180:183], v150 offset:52224
	ds_read_b128 v[184:187], v150 offset:53248
	ds_read_b128 v[190:193], v150 offset:54272
	ds_read_b128 v[194:197], v150 offset:55296
	ds_read_b128 v[198:201], v150 offset:56320
	global_load_lds_dwordx4 v130, s[68:69]
	s_mov_b32 m0, s41
	s_nop 0
	global_load_lds_dwordx4 v134, s[68:69]
	s_barrier
	s_waitcnt lgkmcnt(0)
	s_setprio 1
	s_waitcnt lgkmcnt(0)
	v_mfma_f32_16x16x32_bf16 v[62:65], v[152:155], v[168:171], v[62:65]
	v_mfma_f32_16x16x32_bf16 v[58:61], v[160:163], v[168:171], v[58:61]
	v_mfma_f32_16x16x32_bf16 v[54:57], v[152:155], v[176:179], v[54:57]
	v_mfma_f32_16x16x32_bf16 v[50:53], v[160:163], v[176:179], v[50:53]
	v_mfma_f32_16x16x32_bf16 v[38:41], v[152:155], v[184:187], v[38:41]
	v_mfma_f32_16x16x32_bf16 v[34:37], v[160:163], v[184:187], v[34:37]
	v_mfma_f32_16x16x32_bf16 v[22:25], v[152:155], v[194:197], v[22:25]
	v_mfma_f32_16x16x32_bf16 v[18:21], v[160:163], v[194:197], v[18:21]
	v_mfma_f32_16x16x32_bf16 v[62:65], v[156:159], v[172:175], v[62:65]
	v_mfma_f32_16x16x32_bf16 v[58:61], v[164:167], v[172:175], v[58:61]
	v_mfma_f32_16x16x32_bf16 v[54:57], v[156:159], v[180:183], v[54:57]
	v_mfma_f32_16x16x32_bf16 v[50:53], v[164:167], v[180:183], v[50:53]
	v_mfma_f32_16x16x32_bf16 v[38:41], v[156:159], v[190:193], v[38:41]
	v_mfma_f32_16x16x32_bf16 v[34:37], v[164:167], v[190:193], v[34:37]
	v_mfma_f32_16x16x32_bf16 v[22:25], v[156:159], v[198:201], v[22:25]
	v_mfma_f32_16x16x32_bf16 v[18:21], v[164:167], v[198:201], v[18:21]
	s_setprio 0
	s_barrier
	s_add_u32 s28, s28, 0x80080
	s_addc_u32 s29, s29, 0
	s_add_i32 s30, s30, s35
	s_mov_b32 m0, s30
	s_nop 0
	global_load_lds_dwordx4 v132, s[28:29]
	s_add_i32 m0, s30, 0x2000
	s_nop 0
	global_load_lds_dwordx4 v136, s[28:29]
	s_waitcnt vmcnt(6)
	s_barrier
	s_setprio 1
	v_mfma_f32_16x16x32_bf16 v[46:49], v[214:217], v[168:171], v[46:49]
	v_mfma_f32_16x16x32_bf16 v[42:45], v[222:225], v[168:171], v[42:45]
	v_mfma_f32_16x16x32_bf16 v[30:33], v[214:217], v[176:179], v[30:33]
	v_mfma_f32_16x16x32_bf16 v[26:29], v[222:225], v[176:179], v[26:29]
	v_mfma_f32_16x16x32_bf16 v[14:17], v[214:217], v[184:187], v[14:17]
	v_mfma_f32_16x16x32_bf16 v[10:13], v[222:225], v[184:187], v[10:13]
	v_mfma_f32_16x16x32_bf16 v[6:9], v[214:217], v[194:197], v[6:9]
	v_mfma_f32_16x16x32_bf16 v[2:5], v[222:225], v[194:197], v[2:5]
	v_mfma_f32_16x16x32_bf16 v[46:49], v[218:221], v[172:175], v[46:49]
	v_mfma_f32_16x16x32_bf16 v[42:45], v[226:229], v[172:175], v[42:45]
	v_mfma_f32_16x16x32_bf16 v[30:33], v[218:221], v[180:183], v[30:33]
	v_mfma_f32_16x16x32_bf16 v[26:29], v[226:229], v[180:183], v[26:29]
	v_mfma_f32_16x16x32_bf16 v[14:17], v[218:221], v[190:193], v[14:17]
	v_mfma_f32_16x16x32_bf16 v[10:13], v[226:229], v[190:193], v[10:13]
	v_mfma_f32_16x16x32_bf16 v[6:9], v[218:221], v[198:201], v[6:9]
	v_mfma_f32_16x16x32_bf16 v[2:5], v[226:229], v[198:201], v[2:5]
	s_setprio 0
	s_add_i32 s54, s54, 2
	s_add_u32 s26, s26, 0x100
	s_addc_u32 s27, s27, 0
	s_add_u32 s52, s52, 0x100
	s_addc_u32 s53, s53, 0
	s_cmp_gt_u32 s54, 29
	s_barrier
	s_cbranch_scc0 .LBB0_1369
	v_lshl_add_u32 v152, s16, 8, v146
	v_lshl_or_b32 v154, s49, 8, v148
	v_ashrrev_i32_e32 v153, 31, v152
	v_ashrrev_i32_e32 v155, 31, v154
	v_lshlrev_b64 v[156:157], 12, v[152:153]
	v_lshl_add_u64 v[156:157], s[96:97], 0, v[156:157]
	v_lshlrev_b64 v[154:155], 1, v[154:155]
	v_lshl_add_u64 v[156:157], v[156:157], 0, v[154:155]
	v_cvt_pk_bf16_f32 v62, v62, v63
	v_cvt_pk_bf16_f32 v63, v64, v65
	v_cvt_pk_bf16_f32 v64, v58, v59
	v_add_co_u32_e32 v58, vcc, s45, v156
	v_cvt_pk_bf16_f32 v70, v70, v71
	v_cvt_pk_bf16_f32 v71, v72, v73
	v_cvt_pk_bf16_f32 v72, v66, v67
	v_lshl_add_u64 v[66:67], v[156:157], 0, s[6:7]
	v_addc_co_u32_e32 v59, vcc, 0, v157, vcc
	v_cvt_pk_bf16_f32 v46, v46, v47
	v_cvt_pk_bf16_f32 v47, v48, v49
	v_cvt_pk_bf16_f32 v48, v42, v43
	v_cvt_pk_bf16_f32 v49, v44, v45
	v_cvt_pk_bf16_f32 v110, v110, v111
	v_cvt_pk_bf16_f32 v111, v112, v113
	v_cvt_pk_bf16_f32 v112, v106, v107
	v_or_b32_e32 v106, 16, v152
	global_store_dwordx4 v[66:67], v[46:49], off offset:256
	v_ashrrev_i32_e32 v107, 31, v106
	v_cvt_pk_bf16_f32 v94, v94, v95
	v_add_co_u32_e32 v48, vcc, s46, v156
	v_cvt_pk_bf16_f32 v95, v96, v97
	v_cvt_pk_bf16_f32 v96, v90, v91
	v_or_b32_e32 v90, 32, v152
	v_lshl_add_u64 v[46:47], v[156:157], 0, s[10:11]
	v_addc_co_u32_e32 v49, vcc, 0, v157, vcc
	v_cvt_pk_bf16_f32 v30, v30, v31
	v_cvt_pk_bf16_f32 v31, v32, v33
	v_cvt_pk_bf16_f32 v32, v26, v27
	v_cvt_pk_bf16_f32 v33, v28, v29
	v_lshlrev_b64 v[106:107], 12, v[106:107]
	v_ashrrev_i32_e32 v91, 31, v90
	v_cvt_pk_bf16_f32 v78, v78, v79
	v_cvt_pk_bf16_f32 v79, v80, v81
	v_cvt_pk_bf16_f32 v80, v74, v75
	v_or_b32_e32 v74, 48, v152
	global_store_dwordx4 v[46:47], v[30:33], off offset:256
	v_cvt_pk_bf16_f32 v113, v108, v109
	v_lshl_add_u64 v[106:107], s[96:97], 0, v[106:107]
	v_add_co_u32_e32 v32, vcc, s47, v156
	v_lshlrev_b64 v[90:91], 12, v[90:91]
	v_ashrrev_i32_e32 v75, 31, v74
	v_lshl_add_u64 v[30:31], v[156:157], 0, s[12:13]
	v_addc_co_u32_e32 v33, vcc, 0, v157, vcc
	v_cvt_pk_bf16_f32 v14, v14, v15
	v_cvt_pk_bf16_f32 v15, v16, v17
	v_cvt_pk_bf16_f32 v16, v10, v11
	v_cvt_pk_bf16_f32 v17, v12, v13
	global_store_dwordx4 v[156:157], v[110:113], off offset:256
	v_cvt_pk_bf16_f32 v97, v92, v93
	v_lshl_add_u64 v[90:91], s[96:97], 0, v[90:91]
	v_lshl_add_u64 v[110:111], v[106:107], 0, v[154:155]
	v_lshlrev_b64 v[74:75], 12, v[74:75]
	global_store_dwordx4 v[30:31], v[14:17], off offset:256
	global_store_dwordx4 v[110:111], v[94:97], off offset:256
	v_cvt_pk_bf16_f32 v81, v76, v77
	v_add_co_u32_e32 v16, vcc, s48, v156
	v_lshl_add_u64 v[94:95], v[90:91], 0, v[154:155]
	v_lshl_add_u64 v[74:75], s[96:97], 0, v[74:75]
	v_addc_co_u32_e32 v17, vcc, 0, v157, vcc
	v_cvt_pk_bf16_f32 v126, v126, v127
	v_cvt_pk_bf16_f32 v127, v128, v129
	v_cvt_pk_bf16_f32 v128, v122, v123
	v_cvt_pk_bf16_f32 v129, v124, v125
	v_cvt_pk_bf16_f32 v106, v118, v119
	v_cvt_pk_bf16_f32 v107, v120, v121
	v_cvt_pk_bf16_f32 v108, v114, v115
	v_cvt_pk_bf16_f32 v109, v116, v117
	v_cvt_pk_bf16_f32 v90, v102, v103
	v_cvt_pk_bf16_f32 v91, v104, v105
	v_cvt_pk_bf16_f32 v92, v98, v99
	v_cvt_pk_bf16_f32 v93, v100, v101
	global_store_dwordx4 v[94:95], v[78:81], off offset:256
	v_cvt_pk_bf16_f32 v76, v82, v83
	v_cvt_pk_bf16_f32 v77, v84, v85
	v_lshl_add_u64 v[78:79], v[74:75], 0, v[154:155]
	v_cvt_pk_bf16_f32 v74, v86, v87
	v_cvt_pk_bf16_f32 v75, v88, v89
	v_cvt_pk_bf16_f32 v73, v68, v69
	v_cvt_pk_bf16_f32 v65, v60, v61
	v_cvt_pk_bf16_f32 v42, v54, v55
	v_cvt_pk_bf16_f32 v43, v56, v57
	v_cvt_pk_bf16_f32 v44, v50, v51
	v_cvt_pk_bf16_f32 v45, v52, v53
	v_cvt_pk_bf16_f32 v26, v38, v39
	v_cvt_pk_bf16_f32 v27, v40, v41
	v_cvt_pk_bf16_f32 v28, v34, v35
	v_cvt_pk_bf16_f32 v29, v36, v37
	v_lshl_add_u64 v[14:15], v[156:157], 0, s[14:15]
	v_cvt_pk_bf16_f32 v10, v22, v23
	v_cvt_pk_bf16_f32 v11, v24, v25
	v_cvt_pk_bf16_f32 v12, v18, v19
	v_cvt_pk_bf16_f32 v13, v20, v21
	v_cvt_pk_bf16_f32 v6, v6, v7
	v_cvt_pk_bf16_f32 v7, v8, v9
	v_cvt_pk_bf16_f32 v8, v2, v3
	v_cvt_pk_bf16_f32 v9, v4, v5
	s_and_b64 vcc, exec, s[0:1]
	s_mov_b32 s49, s18
	s_mov_b32 s16, s20
	s_mov_b64 s[28:29], s[24:25]
	s_mov_b64 s[26:27], s[22:23]
	global_store_dwordx4 v[156:157], v[126:129], off
	global_store_dwordx4 v[110:111], v[106:109], off
	global_store_dwordx4 v[94:95], v[90:93], off
	global_store_dwordx4 v[78:79], v[74:77], off
	global_store_dwordx4 v[78:79], v[70:73], off offset:256
	global_store_dwordx4 v[58:59], v[62:65], off
	global_store_dwordx4 v[48:49], v[42:45], off
	global_store_dwordx4 v[32:33], v[26:29], off
	global_store_dwordx4 v[16:17], v[10:13], off
	global_store_dwordx4 v[14:15], v[6:9], off offset:256
	s_cbranch_vccz .LBB0_1362
	s_waitcnt vmcnt(0)
	s_cmpk_gt_u32 s2, 0xff
	s_cbranch_scc1 .LBB0_1373
	s_barrier
